# attention: waves stop computing key tiles that are fully above their query rows (still join barrier and K/V DMA); epilogue lane swaps by DPP instead of ds_bpermute; K LDS swizzle conflict-free
# speedup vs baseline: 1.0209x; 1.0160x over previous
.LBB0_813:
	v_cvt_pk_bf16_f32 v178, v82, v175
	v_cvt_pk_bf16_f32 v179, v84, v85
	v_cvt_pk_bf16_f32 v180, v86, v87
	v_cvt_pk_bf16_f32 v181, v88, v176
	v_cvt_pk_bf16_f32 v84, v89, v90
	v_cvt_pk_bf16_f32 v85, v91, v92
	v_cvt_pk_bf16_f32 v86, v93, v94
	v_cvt_pk_bf16_f32 v87, v95, v96
	v_cvt_pk_bf16_f32 v66, v66, v67
	v_cvt_pk_bf16_f32 v67, v68, v69
	v_cvt_pk_bf16_f32 v68, v70, v71
	v_cvt_pk_bf16_f32 v69, v72, v83
	v_cvt_pk_bf16_f32 v70, v73, v74
	v_cvt_pk_bf16_f32 v71, v75, v76
	v_cvt_pk_bf16_f32 v72, v77, v78
	v_cvt_pk_bf16_f32 v73, v80, v81
	v_lshl_add_u32 v78, s87, 14, v172
	ds_read_b64_tr_b16 v[74:75], v78 offset:0
	ds_read_b64_tr_b16 v[76:77], v78 offset:0x800
	ds_read_b64_tr_b16 v[80:81], v78 offset:0x1000
	ds_read_b64_tr_b16 v[82:83], v78 offset:0x1800
	ds_read_b64_tr_b16 v[88:89], v78 offset:0x2000
	ds_read_b64_tr_b16 v[90:91], v78 offset:0x2800
	ds_read_b64_tr_b16 v[92:93], v78 offset:0x3000
	v_add_f32_e32 v79, v79, v177
	ds_read_b64_tr_b16 v[94:95], v78 offset:0x3800
	v_fmac_f32_e32 v79, v174, v97
	ds_read_b64_tr_b16 v[174:175], v78 offset:0x200
	ds_read_b64_tr_b16 v[176:177], v78 offset:0xa00
	ds_read_b64_tr_b16 v[182:183], v78 offset:0x1200
	ds_read_b64_tr_b16 v[184:185], v78 offset:0x1a00
	ds_read_b64_tr_b16 v[186:187], v78 offset:0x2200
	ds_read_b64_tr_b16 v[188:189], v78 offset:0x2a00
	ds_read_b64_tr_b16 v[190:191], v78 offset:0x3200
	ds_read_b64_tr_b16 v[192:193], v78 offset:0x3a00
	s_waitcnt lgkmcnt(8)
	v_permlane32_swap_b32_e32 v178, v180
	v_permlane32_swap_b32_e32 v179, v181
	v_permlane32_swap_b32_e32 v84, v86
	v_permlane32_swap_b32_e32 v85, v87
	v_permlane32_swap_b32_e32 v66, v68
	v_permlane32_swap_b32_e32 v67, v69
	v_permlane32_swap_b32_e32 v70, v72
	v_permlane32_swap_b32_e32 v71, v73
	v_mfma_f32_32x32x16_bf16 v[50:65], v[178:181], v[74:77], v[50:65]
	ds_read_b64_tr_b16 v[74:75], v78 offset:0x400
	ds_read_b64_tr_b16 v[76:77], v78 offset:0xc00
	v_mfma_f32_32x32x16_bf16 v[50:65], v[84:87], v[80:83], v[50:65]
	ds_read_b64_tr_b16 v[80:81], v78 offset:0x1400
	ds_read_b64_tr_b16 v[82:83], v78 offset:0x1c00
	v_mfma_f32_32x32x16_bf16 v[50:65], v[66:69], v[88:91], v[50:65]
	ds_read_b64_tr_b16 v[88:89], v78 offset:0x2400
	ds_read_b64_tr_b16 v[90:91], v78 offset:0x2c00
	v_mfma_f32_32x32x16_bf16 v[50:65], v[70:73], v[92:95], v[50:65]
	ds_read_b64_tr_b16 v[92:93], v78 offset:0x3400
	ds_read_b64_tr_b16 v[94:95], v78 offset:0x3c00
	s_waitcnt lgkmcnt(8)
	v_mfma_f32_32x32x16_bf16 v[34:49], v[178:181], v[174:177], v[34:49]
	ds_read_b64_tr_b16 v[174:175], v78 offset:0x600
	ds_read_b64_tr_b16 v[176:177], v78 offset:0xe00
	v_mfma_f32_32x32x16_bf16 v[34:49], v[84:87], v[182:185], v[34:49]
	ds_read_b64_tr_b16 v[182:183], v78 offset:0x1600
	ds_read_b64_tr_b16 v[184:185], v78 offset:0x1e00
	v_mfma_f32_32x32x16_bf16 v[34:49], v[66:69], v[186:189], v[34:49]
	ds_read_b64_tr_b16 v[186:187], v78 offset:0x2600
	ds_read_b64_tr_b16 v[188:189], v78 offset:0x2e00
	v_mfma_f32_32x32x16_bf16 v[34:49], v[70:73], v[190:193], v[34:49]
	ds_read_b64_tr_b16 v[190:191], v78 offset:0x3600
	ds_read_b64_tr_b16 v[192:193], v78 offset:0x3e00
	s_waitcnt lgkmcnt(8)
	v_mfma_f32_32x32x16_bf16 v[18:33], v[178:181], v[74:77], v[18:33]
	s_waitcnt lgkmcnt(0)
	v_mfma_f32_32x32x16_bf16 v[18:33], v[84:87], v[80:83], v[18:33]
	v_mfma_f32_32x32x16_bf16 v[18:33], v[66:69], v[88:91], v[18:33]
	v_mfma_f32_32x32x16_bf16 v[18:33], v[70:73], v[92:95], v[18:33]
	v_mfma_f32_32x32x16_bf16 v[2:17], v[178:181], v[174:177], v[2:17]
	s_add_i32 s86, s86, 64
	s_add_i32 s12, s12, 1
	v_lshl_add_u64 v[150:151], v[150:151], 0, s[14:15]
	v_lshl_add_u64 v[152:153], v[152:153], 0, s[14:15]
	v_lshl_add_u64 v[154:155], v[154:155], 0, s[16:17]
	v_lshl_add_u64 v[156:157], v[156:157], 0, s[16:17]
	v_lshl_add_u64 v[158:159], v[158:159], 0, s[16:17]
	v_mfma_f32_32x32x16_bf16 v[2:17], v[84:87], v[182:185], v[2:17]
	v_subrev_u32_e32 v168, 64, v168
	s_cmp_eq_u32 s83, s86
	v_mfma_f32_32x32x16_bf16 v[2:17], v[66:69], v[186:189], v[2:17]
	v_mfma_f32_32x32x16_bf16 v[2:17], v[70:73], v[190:193], v[2:17]
	s_cbranch_scc1 .LBB0_815
	v_mov_b32_e32 v174, v79
	s_add_i32 s56, s86, 0xe0
	s_cmp_ge_i32 s56, s84
	s_cbranch_scc0 .LBB0_805

.Latt1_drain_nodma:
	s_add_i32 s86, s86, 64
	s_add_i32 s12, s12, 1
	v_lshl_add_u64 v[150:151], v[150:151], 0, s[14:15]
	v_lshl_add_u64 v[152:153], v[152:153], 0, s[14:15]
	v_lshl_add_u64 v[154:155], v[154:155], 0, s[16:17]
	v_lshl_add_u64 v[156:157], v[156:157], 0, s[16:17]
	v_lshl_add_u64 v[158:159], v[158:159], 0, s[16:17]
	s_cmp_eq_u32 s83, s86
	s_cbranch_scc0 .Latt1_drain
	s_branch .LBB0_815

.LBB0_817:
	s_or_b64 exec, exec, s[56:57]
	v_and_b32_e32 v68, 64, v164
	v_xor_b32_e32 v67, 1, v164
	v_add_u32_e32 v68, 64, v68
	v_cmp_lt_i32_e32 vcc, v67, v68
	s_waitcnt lgkmcnt(0)
	s_lshl_b64 s[0:1], s[54:55], 11
	v_ashrrev_i32_e32 v73, 3, v167
	v_cndmask_b32_e32 v67, v164, v67, vcc
	v_lshlrev_b32_e32 v160, 2, v67
	v_xor_b32_e32 v67, 2, v164
	v_cmp_lt_i32_e32 vcc, v67, v68
	v_and_b32_e32 v66, -4, v73
	v_lshl_add_u32 v72, v66, 2, s65
	v_cndmask_b32_e32 v67, v164, v67, vcc
	v_lshlrev_b32_e32 v161, 2, v67
	v_and_b32_e32 v67, 3, v167
	v_cmp_eq_u32_e32 vcc, 0, v67
	ds_read_b32 v67, v72 offset:128
	s_add_u32 s0, s61, s0
	s_addc_u32 s1, s62, s1
	s_add_u32 s0, s0, s79
	v_and_b32_e32 v148, 31, v167
	s_waitcnt lgkmcnt(0)
	v_mul_f32_e32 v74, 0x41800000, v67
	v_mul_f32_e32 v75, v50, v74
	s_nop 1
	v_mov_b32_dpp v50, v75 quad_perm:[1,0,3,2] row_mask:0xf bank_mask:0xf
	s_nop 1
	v_mov_b32_dpp v77, v75 quad_perm:[2,3,0,1] row_mask:0xf bank_mask:0xf
	s_addc_u32 s1, s1, 0
	v_ashrrev_i32_e32 v67, 31, v66
	v_lshl_add_u64 v[68:69], s[0:1], 0, v[148:149]
	s_waitcnt lgkmcnt(0)
	s_nop 1
	v_mov_b32_dpp v76, v50 quad_perm:[2,3,0,1] row_mask:0xf bank_mask:0xf
	v_lshlrev_b64 v[70:71], 11, v[66:67]
	v_lshl_add_u64 v[70:71], v[68:69], 0, v[70:71]
	s_and_saveexec_b64 s[0:1], vcc
	s_cbranch_execz .LBB0_819
	v_max_f32_e32 v75, v75, v75
	v_max_f32_e32 v50, v50, v50
	v_med3_f32 v75, v75, s77, v166
	v_med3_f32 v50, v50, s77, v166
	v_mov_b32_e32 v78, v149
	v_cvt_pk_fp8_f32 v78, v75, v50
	v_max_f32_e32 v77, v77, v77
	s_waitcnt lgkmcnt(0)
	v_max_f32_e32 v75, v76, v76
	v_med3_f32 v50, v77, s77, v166
	v_med3_f32 v75, v75, s77, v166
	v_cvt_pk_fp8_f32 v78, v50, v75 op_sel:[0,0,1]
	global_store_dword v[70:71], v78, off
.LBB0_819:
	s_or_b64 exec, exec, s[0:1]
	s_waitcnt lgkmcnt(0)
	v_mul_f32_e32 v76, v34, v74
	s_nop 1
	v_mov_b32_dpp v75, v76 quad_perm:[1,0,3,2] row_mask:0xf bank_mask:0xf
	s_nop 1
	v_mov_b32_dpp v50, v76 quad_perm:[2,3,0,1] row_mask:0xf bank_mask:0xf
	s_waitcnt lgkmcnt(0)
	s_nop 1
	v_mov_b32_dpp v34, v75 quad_perm:[2,3,0,1] row_mask:0xf bank_mask:0xf
	s_and_saveexec_b64 s[0:1], vcc
	s_cbranch_execz .LBB0_821
	v_max_f32_e32 v76, v76, v76
	v_max_f32_e32 v75, v75, v75
	v_med3_f32 v76, v76, s77, v166
	v_med3_f32 v75, v75, s77, v166
	v_mov_b32_e32 v77, v149
	v_cvt_pk_fp8_f32 v77, v76, v75
	v_max_f32_e32 v50, v50, v50
	s_waitcnt lgkmcnt(0)
	v_max_f32_e32 v34, v34, v34
	v_med3_f32 v50, v50, s77, v166
	v_med3_f32 v34, v34, s77, v166
	v_cvt_pk_fp8_f32 v77, v50, v34 op_sel:[0,0,1]
	global_store_dword v[70:71], v77, off offset:32
.LBB0_821:
	s_or_b64 exec, exec, s[0:1]
	v_mul_f32_e32 v75, v18, v74
	s_nop 1
	v_mov_b32_dpp v50, v75 quad_perm:[1,0,3,2] row_mask:0xf bank_mask:0xf
	s_waitcnt lgkmcnt(0)
	s_nop 1
	v_mov_b32_dpp v34, v75 quad_perm:[2,3,0,1] row_mask:0xf bank_mask:0xf
	s_nop 1
	v_mov_b32_dpp v18, v50 quad_perm:[2,3,0,1] row_mask:0xf bank_mask:0xf
	s_and_saveexec_b64 s[0:1], vcc
	s_cbranch_execz .LBB0_823
	v_max_f32_e32 v75, v75, v75
	v_max_f32_e32 v50, v50, v50
	v_med3_f32 v75, v75, s77, v166
	v_med3_f32 v50, v50, s77, v166
	v_mov_b32_e32 v76, v149
	v_cvt_pk_fp8_f32 v76, v75, v50
	s_waitcnt lgkmcnt(0)
	v_max_f32_e32 v34, v34, v34
	v_max_f32_e32 v18, v18, v18
	v_med3_f32 v34, v34, s77, v166
	v_med3_f32 v18, v18, s77, v166
	v_cvt_pk_fp8_f32 v76, v34, v18 op_sel:[0,0,1]
	global_store_dword v[70:71], v76, off offset:64
.LBB0_823:
	s_or_b64 exec, exec, s[0:1]
	v_mul_f32_e32 v50, v2, v74
	s_waitcnt lgkmcnt(0)
	s_nop 1
	v_mov_b32_dpp v34, v50 quad_perm:[1,0,3,2] row_mask:0xf bank_mask:0xf
	s_nop 1
	v_mov_b32_dpp v18, v50 quad_perm:[2,3,0,1] row_mask:0xf bank_mask:0xf
	s_waitcnt lgkmcnt(0)
	s_nop 1
	v_mov_b32_dpp v2, v34 quad_perm:[2,3,0,1] row_mask:0xf bank_mask:0xf
	s_and_saveexec_b64 s[0:1], vcc
	s_cbranch_execz .LBB0_825
	v_max_f32_e32 v50, v50, v50
	v_max_f32_e32 v34, v34, v34
	v_med3_f32 v50, v50, s77, v166
	v_med3_f32 v34, v34, s77, v166
	v_mov_b32_e32 v74, v149
	v_cvt_pk_fp8_f32 v74, v50, v34
	v_max_f32_e32 v18, v18, v18
	s_waitcnt lgkmcnt(0)
	v_max_f32_e32 v2, v2, v2
	v_med3_f32 v18, v18, s77, v166
	v_med3_f32 v2, v2, s77, v166
	v_cvt_pk_fp8_f32 v74, v18, v2 op_sel:[0,0,1]
	global_store_dword v[70:71], v74, off offset:96
.LBB0_825:
	s_or_b64 exec, exec, s[0:1]
	s_waitcnt lgkmcnt(0)
	ds_read_b32 v2, v72 offset:132
	v_or_b32_e32 v70, 1, v66
	v_ashrrev_i32_e32 v71, 31, v70
	v_lshlrev_b64 v[70:71], 11, v[70:71]
	v_lshl_add_u64 v[70:71], v[68:69], 0, v[70:71]
	s_waitcnt lgkmcnt(0)
	v_mul_f32_e32 v2, 0x41800000, v2
	v_mul_f32_e32 v51, v51, v2
	s_nop 1
	v_mov_b32_dpp v50, v51 quad_perm:[1,0,3,2] row_mask:0xf bank_mask:0xf
	s_nop 1
	v_mov_b32_dpp v34, v51 quad_perm:[2,3,0,1] row_mask:0xf bank_mask:0xf
	s_waitcnt lgkmcnt(0)
	s_nop 1
	v_mov_b32_dpp v18, v50 quad_perm:[2,3,0,1] row_mask:0xf bank_mask:0xf
	s_and_saveexec_b64 s[0:1], vcc
	s_cbranch_execz .LBB0_827
	v_max_f32_e32 v51, v51, v51
	v_max_f32_e32 v50, v50, v50
	v_med3_f32 v51, v51, s77, v166
	v_med3_f32 v50, v50, s77, v166
	v_mov_b32_e32 v74, v149
	v_cvt_pk_fp8_f32 v74, v51, v50
	v_max_f32_e32 v34, v34, v34
	s_waitcnt lgkmcnt(0)
	v_max_f32_e32 v18, v18, v18
	v_med3_f32 v34, v34, s77, v166
	v_med3_f32 v18, v18, s77, v166
	v_cvt_pk_fp8_f32 v74, v34, v18 op_sel:[0,0,1]
	global_store_dword v[70:71], v74, off
.LBB0_827:
	s_or_b64 exec, exec, s[0:1]
	v_mul_f32_e32 v50, v35, v2
	s_nop 1
	v_mov_b32_dpp v35, v50 quad_perm:[1,0,3,2] row_mask:0xf bank_mask:0xf
	s_nop 1
	v_mov_b32_dpp v34, v50 quad_perm:[2,3,0,1] row_mask:0xf bank_mask:0xf
	s_waitcnt lgkmcnt(0)
	s_nop 1
	v_mov_b32_dpp v18, v35 quad_perm:[2,3,0,1] row_mask:0xf bank_mask:0xf
	s_and_saveexec_b64 s[0:1], vcc
	s_cbranch_execz .LBB0_829
	v_max_f32_e32 v50, v50, v50
	v_max_f32_e32 v35, v35, v35
	v_med3_f32 v50, v50, s77, v166
	v_med3_f32 v35, v35, s77, v166
	v_mov_b32_e32 v51, v149
	v_cvt_pk_fp8_f32 v51, v50, v35
	v_max_f32_e32 v34, v34, v34
	s_waitcnt lgkmcnt(0)
	v_max_f32_e32 v18, v18, v18
	v_med3_f32 v34, v34, s77, v166
	v_med3_f32 v18, v18, s77, v166
	v_cvt_pk_fp8_f32 v51, v34, v18 op_sel:[0,0,1]
	global_store_dword v[70:71], v51, off offset:32
.LBB0_829:
	s_or_b64 exec, exec, s[0:1]
	v_mul_f32_e32 v35, v19, v2
	s_nop 1
	v_mov_b32_dpp v34, v35 quad_perm:[1,0,3,2] row_mask:0xf bank_mask:0xf
	s_nop 1
	v_mov_b32_dpp v19, v35 quad_perm:[2,3,0,1] row_mask:0xf bank_mask:0xf
	s_waitcnt lgkmcnt(0)
	s_nop 1
	v_mov_b32_dpp v18, v34 quad_perm:[2,3,0,1] row_mask:0xf bank_mask:0xf
	s_and_saveexec_b64 s[0:1], vcc
	s_cbranch_execz .LBB0_831
	v_max_f32_e32 v35, v35, v35
	v_max_f32_e32 v34, v34, v34
	v_med3_f32 v35, v35, s77, v166
	v_med3_f32 v34, v34, s77, v166
	v_mov_b32_e32 v50, v149
	v_cvt_pk_fp8_f32 v50, v35, v34
	v_max_f32_e32 v19, v19, v19
	s_waitcnt lgkmcnt(0)
	v_max_f32_e32 v18, v18, v18
	v_med3_f32 v19, v19, s77, v166
	v_med3_f32 v18, v18, s77, v166
	v_cvt_pk_fp8_f32 v50, v19, v18 op_sel:[0,0,1]
	global_store_dword v[70:71], v50, off offset:64
.LBB0_831:
	s_or_b64 exec, exec, s[0:1]
	v_mul_f32_e32 v19, v3, v2
	s_waitcnt lgkmcnt(0)
	s_nop 1
	v_mov_b32_dpp v18, v19 quad_perm:[1,0,3,2] row_mask:0xf bank_mask:0xf
	s_nop 1
	v_mov_b32_dpp v3, v19 quad_perm:[2,3,0,1] row_mask:0xf bank_mask:0xf
	s_waitcnt lgkmcnt(0)
	s_nop 1
	v_mov_b32_dpp v2, v18 quad_perm:[2,3,0,1] row_mask:0xf bank_mask:0xf
	s_and_saveexec_b64 s[0:1], vcc
	s_cbranch_execz .LBB0_833
	v_max_f32_e32 v19, v19, v19
	v_max_f32_e32 v18, v18, v18
	v_med3_f32 v19, v19, s77, v166
	v_med3_f32 v18, v18, s77, v166
	v_mov_b32_e32 v34, v149
	v_cvt_pk_fp8_f32 v34, v19, v18
	v_max_f32_e32 v3, v3, v3
	s_waitcnt lgkmcnt(0)
	v_max_f32_e32 v2, v2, v2
	v_med3_f32 v3, v3, s77, v166
	v_med3_f32 v2, v2, s77, v166
	v_cvt_pk_fp8_f32 v34, v3, v2 op_sel:[0,0,1]
	global_store_dword v[70:71], v34, off offset:96
.LBB0_833:
	s_or_b64 exec, exec, s[0:1]
	ds_read_b32 v3, v72 offset:136
	s_waitcnt lgkmcnt(0)
	v_or_b32_e32 v2, 2, v66
	v_mul_f32_e32 v18, 0x41800000, v3
	v_mul_f32_e32 v50, v52, v18
	s_nop 1
	v_mov_b32_dpp v35, v50 quad_perm:[1,0,3,2] row_mask:0xf bank_mask:0xf
	s_nop 1
	v_mov_b32_dpp v34, v50 quad_perm:[2,3,0,1] row_mask:0xf bank_mask:0xf
	v_ashrrev_i32_e32 v3, 31, v2
	v_lshlrev_b64 v[2:3], 11, v[2:3]
	v_lshl_add_u64 v[2:3], v[68:69], 0, v[2:3]
	s_waitcnt lgkmcnt(0)
	s_nop 1
	v_mov_b32_dpp v19, v35 quad_perm:[2,3,0,1] row_mask:0xf bank_mask:0xf
	s_and_saveexec_b64 s[0:1], vcc
	s_cbranch_execz .LBB0_835
	v_max_f32_e32 v50, v50, v50
	v_max_f32_e32 v35, v35, v35
	v_med3_f32 v50, v50, s77, v166
	v_med3_f32 v35, v35, s77, v166
	v_mov_b32_e32 v51, v149
	v_cvt_pk_fp8_f32 v51, v50, v35
	v_max_f32_e32 v34, v34, v34
	s_waitcnt lgkmcnt(0)
	v_max_f32_e32 v19, v19, v19
	v_med3_f32 v34, v34, s77, v166
	v_med3_f32 v19, v19, s77, v166
	v_cvt_pk_fp8_f32 v51, v34, v19 op_sel:[0,0,1]
	global_store_dword v[2:3], v51, off
.LBB0_835:
	s_or_b64 exec, exec, s[0:1]
	v_mul_f32_e32 v36, v36, v18
	s_nop 1
	v_mov_b32_dpp v35, v36 quad_perm:[1,0,3,2] row_mask:0xf bank_mask:0xf
	s_nop 1
	v_mov_b32_dpp v34, v36 quad_perm:[2,3,0,1] row_mask:0xf bank_mask:0xf
	s_waitcnt lgkmcnt(0)
	s_nop 1
	v_mov_b32_dpp v19, v35 quad_perm:[2,3,0,1] row_mask:0xf bank_mask:0xf
	s_and_saveexec_b64 s[0:1], vcc
	s_cbranch_execz .LBB0_837
	v_max_f32_e32 v36, v36, v36
	v_max_f32_e32 v35, v35, v35
	v_med3_f32 v36, v36, s77, v166
	v_med3_f32 v35, v35, s77, v166
	v_mov_b32_e32 v50, v149
	v_cvt_pk_fp8_f32 v50, v36, v35
	v_max_f32_e32 v34, v34, v34
	s_waitcnt lgkmcnt(0)
	v_max_f32_e32 v19, v19, v19
	v_med3_f32 v34, v34, s77, v166
	v_med3_f32 v19, v19, s77, v166
	v_cvt_pk_fp8_f32 v50, v34, v19 op_sel:[0,0,1]
	global_store_dword v[2:3], v50, off offset:32
.LBB0_837:
	s_or_b64 exec, exec, s[0:1]
	v_mul_f32_e32 v35, v20, v18
	s_nop 1
	v_mov_b32_dpp v34, v35 quad_perm:[1,0,3,2] row_mask:0xf bank_mask:0xf
	s_nop 1
	v_mov_b32_dpp v20, v35 quad_perm:[2,3,0,1] row_mask:0xf bank_mask:0xf
	s_waitcnt lgkmcnt(0)
	s_nop 1
	v_mov_b32_dpp v19, v34 quad_perm:[2,3,0,1] row_mask:0xf bank_mask:0xf
	s_and_saveexec_b64 s[0:1], vcc
	s_cbranch_execz .LBB0_839
	v_max_f32_e32 v35, v35, v35
	v_max_f32_e32 v34, v34, v34
	v_med3_f32 v35, v35, s77, v166
	v_med3_f32 v34, v34, s77, v166
	v_mov_b32_e32 v36, v149
	v_cvt_pk_fp8_f32 v36, v35, v34
	v_max_f32_e32 v20, v20, v20
	s_waitcnt lgkmcnt(0)
	v_max_f32_e32 v19, v19, v19
	v_med3_f32 v20, v20, s77, v166
	v_med3_f32 v19, v19, s77, v166
	v_cvt_pk_fp8_f32 v36, v20, v19 op_sel:[0,0,1]
	global_store_dword v[2:3], v36, off offset:64
.LBB0_839:
	s_or_b64 exec, exec, s[0:1]
	v_mul_f32_e32 v20, v4, v18
	s_waitcnt lgkmcnt(0)
	s_nop 1
	v_mov_b32_dpp v19, v20 quad_perm:[1,0,3,2] row_mask:0xf bank_mask:0xf
	s_nop 1
	v_mov_b32_dpp v18, v20 quad_perm:[2,3,0,1] row_mask:0xf bank_mask:0xf
	s_waitcnt lgkmcnt(0)
	s_nop 1
	v_mov_b32_dpp v4, v19 quad_perm:[2,3,0,1] row_mask:0xf bank_mask:0xf
	s_and_saveexec_b64 s[0:1], vcc
	s_cbranch_execz .LBB0_841
	v_max_f32_e32 v20, v20, v20
	v_max_f32_e32 v19, v19, v19
	v_med3_f32 v20, v20, s77, v166
	v_med3_f32 v19, v19, s77, v166
	v_mov_b32_e32 v34, v149
	v_cvt_pk_fp8_f32 v34, v20, v19
	v_max_f32_e32 v18, v18, v18
	s_waitcnt lgkmcnt(0)
	v_max_f32_e32 v4, v4, v4
	v_med3_f32 v18, v18, s77, v166
	v_med3_f32 v4, v4, s77, v166
	v_cvt_pk_fp8_f32 v34, v18, v4 op_sel:[0,0,1]
	global_store_dword v[2:3], v34, off offset:96
.LBB0_841:
	s_or_b64 exec, exec, s[0:1]
	v_or_b32_e32 v2, 3, v73
	v_lshl_add_u32 v3, v2, 2, s65
	ds_read_b32 v3, v3 offset:128
	s_waitcnt lgkmcnt(0)
	v_mul_f32_e32 v4, 0x41800000, v3
	v_mul_f32_e32 v34, v53, v4
	s_nop 1
	v_mov_b32_dpp v20, v34 quad_perm:[1,0,3,2] row_mask:0xf bank_mask:0xf
	s_nop 1
	v_mov_b32_dpp v19, v34 quad_perm:[2,3,0,1] row_mask:0xf bank_mask:0xf
	v_ashrrev_i32_e32 v3, 31, v2
	v_lshlrev_b64 v[2:3], 11, v[2:3]
	v_lshl_add_u64 v[2:3], v[68:69], 0, v[2:3]
	s_waitcnt lgkmcnt(0)
	s_nop 1
	v_mov_b32_dpp v18, v20 quad_perm:[2,3,0,1] row_mask:0xf bank_mask:0xf
	s_and_saveexec_b64 s[0:1], vcc
	s_cbranch_execz .LBB0_843
	v_max_f32_e32 v34, v34, v34
	v_max_f32_e32 v20, v20, v20
	v_med3_f32 v34, v34, s77, v166
	v_med3_f32 v20, v20, s77, v166
	v_mov_b32_e32 v35, v149
	v_cvt_pk_fp8_f32 v35, v34, v20
	v_max_f32_e32 v19, v19, v19
	s_waitcnt lgkmcnt(0)
	v_max_f32_e32 v18, v18, v18
	v_med3_f32 v19, v19, s77, v166
	v_med3_f32 v18, v18, s77, v166
	v_cvt_pk_fp8_f32 v35, v19, v18 op_sel:[0,0,1]
	global_store_dword v[2:3], v35, off
.LBB0_843:
	s_or_b64 exec, exec, s[0:1]
	v_mul_f32_e32 v34, v37, v4
	s_nop 1
	v_mov_b32_dpp v20, v34 quad_perm:[1,0,3,2] row_mask:0xf bank_mask:0xf
	s_nop 1
	v_mov_b32_dpp v19, v34 quad_perm:[2,3,0,1] row_mask:0xf bank_mask:0xf
	s_waitcnt lgkmcnt(0)
	s_nop 1
	v_mov_b32_dpp v18, v20 quad_perm:[2,3,0,1] row_mask:0xf bank_mask:0xf
	s_and_saveexec_b64 s[0:1], vcc
	s_cbranch_execz .LBB0_845
	v_max_f32_e32 v34, v34, v34
	v_max_f32_e32 v20, v20, v20
	v_med3_f32 v34, v34, s77, v166
	v_med3_f32 v20, v20, s77, v166
	v_mov_b32_e32 v35, v149
	v_cvt_pk_fp8_f32 v35, v34, v20
	v_max_f32_e32 v19, v19, v19
	s_waitcnt lgkmcnt(0)
	v_max_f32_e32 v18, v18, v18
	v_med3_f32 v19, v19, s77, v166
	v_med3_f32 v18, v18, s77, v166
	v_cvt_pk_fp8_f32 v35, v19, v18 op_sel:[0,0,1]
	global_store_dword v[2:3], v35, off offset:32
.LBB0_845:
	s_or_b64 exec, exec, s[0:1]
	v_mul_f32_e32 v21, v21, v4
	s_nop 1
	v_mov_b32_dpp v20, v21 quad_perm:[1,0,3,2] row_mask:0xf bank_mask:0xf
	s_nop 1
	v_mov_b32_dpp v19, v21 quad_perm:[2,3,0,1] row_mask:0xf bank_mask:0xf
	s_waitcnt lgkmcnt(0)
	s_nop 1
	v_mov_b32_dpp v18, v20 quad_perm:[2,3,0,1] row_mask:0xf bank_mask:0xf
	s_and_saveexec_b64 s[0:1], vcc
	s_cbranch_execz .LBB0_847
	v_max_f32_e32 v21, v21, v21
	v_max_f32_e32 v20, v20, v20
	v_med3_f32 v21, v21, s77, v166
	v_med3_f32 v20, v20, s77, v166
	v_mov_b32_e32 v34, v149
	v_cvt_pk_fp8_f32 v34, v21, v20
	v_max_f32_e32 v19, v19, v19
	s_waitcnt lgkmcnt(0)
	v_max_f32_e32 v18, v18, v18
	v_med3_f32 v19, v19, s77, v166
	v_med3_f32 v18, v18, s77, v166
	v_cvt_pk_fp8_f32 v34, v19, v18 op_sel:[0,0,1]
	global_store_dword v[2:3], v34, off offset:64
.LBB0_847:
	s_or_b64 exec, exec, s[0:1]
	v_mul_f32_e32 v19, v5, v4
	s_waitcnt lgkmcnt(0)
	s_nop 1
	v_mov_b32_dpp v18, v19 quad_perm:[1,0,3,2] row_mask:0xf bank_mask:0xf
	s_nop 1
	v_mov_b32_dpp v5, v19 quad_perm:[2,3,0,1] row_mask:0xf bank_mask:0xf
	s_waitcnt lgkmcnt(0)
	s_nop 1
	v_mov_b32_dpp v4, v18 quad_perm:[2,3,0,1] row_mask:0xf bank_mask:0xf
	s_and_saveexec_b64 s[0:1], vcc
	s_cbranch_execz .LBB0_849
	v_max_f32_e32 v19, v19, v19
	v_max_f32_e32 v18, v18, v18
	v_med3_f32 v19, v19, s77, v166
	v_med3_f32 v18, v18, s77, v166
	v_mov_b32_e32 v20, v149
	v_cvt_pk_fp8_f32 v20, v19, v18
	v_max_f32_e32 v5, v5, v5
	s_waitcnt lgkmcnt(0)
	v_max_f32_e32 v4, v4, v4
	v_med3_f32 v5, v5, s77, v166
	v_med3_f32 v4, v4, s77, v166
	v_cvt_pk_fp8_f32 v20, v5, v4 op_sel:[0,0,1]
	global_store_dword v[2:3], v20, off offset:96
.LBB0_849:
	s_or_b64 exec, exec, s[0:1]
	ds_read_b32 v2, v72 offset:160
	s_waitcnt lgkmcnt(0)
	v_mul_f32_e32 v4, 0x41800000, v2
	v_mul_f32_e32 v20, v54, v4
	s_nop 1
	v_mov_b32_dpp v19, v20 quad_perm:[1,0,3,2] row_mask:0xf bank_mask:0xf
	s_nop 1
	v_mov_b32_dpp v18, v20 quad_perm:[2,3,0,1] row_mask:0xf bank_mask:0xf
	v_lshlrev_b64 v[2:3], 11, v[66:67]
	v_lshl_add_u64 v[2:3], v[68:69], 0, v[2:3]
	v_lshl_add_u64 v[2:3], v[2:3], 0, s[18:19]
	s_waitcnt lgkmcnt(0)
	s_nop 1
	v_mov_b32_dpp v5, v19 quad_perm:[2,3,0,1] row_mask:0xf bank_mask:0xf
	s_and_saveexec_b64 s[0:1], vcc
	s_cbranch_execz .LBB0_851
	v_max_f32_e32 v20, v20, v20
	v_max_f32_e32 v19, v19, v19
	v_med3_f32 v20, v20, s77, v166
	v_med3_f32 v19, v19, s77, v166
	v_mov_b32_e32 v21, v149
	v_cvt_pk_fp8_f32 v21, v20, v19
	v_max_f32_e32 v18, v18, v18
	s_waitcnt lgkmcnt(0)
	v_max_f32_e32 v5, v5, v5
	v_med3_f32 v18, v18, s77, v166
	v_med3_f32 v5, v5, s77, v166
	v_cvt_pk_fp8_f32 v21, v18, v5 op_sel:[0,0,1]
	global_store_dword v[2:3], v21, off
.LBB0_851:
	s_or_b64 exec, exec, s[0:1]
	v_mul_f32_e32 v20, v38, v4
	s_nop 1
	v_mov_b32_dpp v19, v20 quad_perm:[1,0,3,2] row_mask:0xf bank_mask:0xf
	s_nop 1
	v_mov_b32_dpp v18, v20 quad_perm:[2,3,0,1] row_mask:0xf bank_mask:0xf
	s_waitcnt lgkmcnt(0)
	s_nop 1
	v_mov_b32_dpp v5, v19 quad_perm:[2,3,0,1] row_mask:0xf bank_mask:0xf
	s_and_saveexec_b64 s[0:1], vcc
	s_cbranch_execz .LBB0_853
	v_max_f32_e32 v20, v20, v20
	v_max_f32_e32 v19, v19, v19
	v_med3_f32 v20, v20, s77, v166
	v_med3_f32 v19, v19, s77, v166
	v_mov_b32_e32 v21, v149
	v_cvt_pk_fp8_f32 v21, v20, v19
	v_max_f32_e32 v18, v18, v18
	s_waitcnt lgkmcnt(0)
	v_max_f32_e32 v5, v5, v5
	v_med3_f32 v18, v18, s77, v166
	v_med3_f32 v5, v5, s77, v166
	v_cvt_pk_fp8_f32 v21, v18, v5 op_sel:[0,0,1]
	global_store_dword v[2:3], v21, off offset:32
.LBB0_853:
	s_or_b64 exec, exec, s[0:1]
	v_mul_f32_e32 v20, v22, v4
	s_nop 1
	v_mov_b32_dpp v19, v20 quad_perm:[1,0,3,2] row_mask:0xf bank_mask:0xf
	s_nop 1
	v_mov_b32_dpp v18, v20 quad_perm:[2,3,0,1] row_mask:0xf bank_mask:0xf
	s_waitcnt lgkmcnt(0)
	s_nop 1
	v_mov_b32_dpp v5, v19 quad_perm:[2,3,0,1] row_mask:0xf bank_mask:0xf
	s_and_saveexec_b64 s[0:1], vcc
	s_cbranch_execz .LBB0_855
	v_max_f32_e32 v20, v20, v20
	v_max_f32_e32 v19, v19, v19
	v_med3_f32 v20, v20, s77, v166
	v_med3_f32 v19, v19, s77, v166
	v_mov_b32_e32 v21, v149
	v_cvt_pk_fp8_f32 v21, v20, v19
	v_max_f32_e32 v18, v18, v18
	s_waitcnt lgkmcnt(0)
	v_max_f32_e32 v5, v5, v5
	v_med3_f32 v18, v18, s77, v166
	v_med3_f32 v5, v5, s77, v166
	v_cvt_pk_fp8_f32 v21, v18, v5 op_sel:[0,0,1]
	global_store_dword v[2:3], v21, off offset:64
.LBB0_855:
	s_or_b64 exec, exec, s[0:1]
	v_mul_f32_e32 v18, v6, v4
	s_nop 1
	v_mov_b32_dpp v6, v18 quad_perm:[1,0,3,2] row_mask:0xf bank_mask:0xf
	s_waitcnt lgkmcnt(0)
	s_nop 1
	v_mov_b32_dpp v5, v18 quad_perm:[2,3,0,1] row_mask:0xf bank_mask:0xf
	s_nop 1
	v_mov_b32_dpp v4, v6 quad_perm:[2,3,0,1] row_mask:0xf bank_mask:0xf
	s_and_saveexec_b64 s[0:1], vcc
	s_cbranch_execz .LBB0_857
	v_max_f32_e32 v18, v18, v18
	v_max_f32_e32 v6, v6, v6
	v_med3_f32 v18, v18, s77, v166
	v_med3_f32 v6, v6, s77, v166
	v_mov_b32_e32 v19, v149
	v_cvt_pk_fp8_f32 v19, v18, v6
	s_waitcnt lgkmcnt(0)
	v_max_f32_e32 v5, v5, v5
	v_max_f32_e32 v4, v4, v4
	v_med3_f32 v5, v5, s77, v166
	v_med3_f32 v4, v4, s77, v166
	v_cvt_pk_fp8_f32 v19, v5, v4 op_sel:[0,0,1]
	global_store_dword v[2:3], v19, off offset:96
.LBB0_857:
	s_or_b64 exec, exec, s[0:1]
	ds_read_b32 v2, v72 offset:164
	s_waitcnt lgkmcnt(0)
	v_mul_f32_e32 v4, 0x41800000, v2
	v_mul_f32_e32 v19, v55, v4
	s_nop 1
	v_mov_b32_dpp v18, v19 quad_perm:[1,0,3,2] row_mask:0xf bank_mask:0xf
	s_nop 1
	v_mov_b32_dpp v6, v19 quad_perm:[2,3,0,1] row_mask:0xf bank_mask:0xf
	v_lshlrev_b64 v[2:3], 11, v[66:67]
	v_lshl_add_u64 v[2:3], v[68:69], 0, v[2:3]
	v_lshl_add_u64 v[2:3], v[2:3], 0, s[20:21]
	s_waitcnt lgkmcnt(0)
	s_nop 1
	v_mov_b32_dpp v5, v18 quad_perm:[2,3,0,1] row_mask:0xf bank_mask:0xf
	s_and_saveexec_b64 s[0:1], vcc
	s_cbranch_execz .LBB0_859
	v_max_f32_e32 v19, v19, v19
	v_max_f32_e32 v18, v18, v18
	v_med3_f32 v19, v19, s77, v166
	v_med3_f32 v18, v18, s77, v166
	v_mov_b32_e32 v20, v149
	v_cvt_pk_fp8_f32 v20, v19, v18
	v_max_f32_e32 v6, v6, v6
	s_waitcnt lgkmcnt(0)
	v_max_f32_e32 v5, v5, v5
	v_med3_f32 v6, v6, s77, v166
	v_med3_f32 v5, v5, s77, v166
	v_cvt_pk_fp8_f32 v20, v6, v5 op_sel:[0,0,1]
	global_store_dword v[2:3], v20, off
.LBB0_859:
	s_or_b64 exec, exec, s[0:1]
	v_mul_f32_e32 v19, v39, v4
	s_nop 1
	v_mov_b32_dpp v18, v19 quad_perm:[1,0,3,2] row_mask:0xf bank_mask:0xf
	s_nop 1
	v_mov_b32_dpp v6, v19 quad_perm:[2,3,0,1] row_mask:0xf bank_mask:0xf
	s_waitcnt lgkmcnt(0)
	s_nop 1
	v_mov_b32_dpp v5, v18 quad_perm:[2,3,0,1] row_mask:0xf bank_mask:0xf
	s_and_saveexec_b64 s[0:1], vcc
	s_cbranch_execz .LBB0_861
	v_max_f32_e32 v19, v19, v19
	v_max_f32_e32 v18, v18, v18
	v_med3_f32 v19, v19, s77, v166
	v_med3_f32 v18, v18, s77, v166
	v_mov_b32_e32 v20, v149
	v_cvt_pk_fp8_f32 v20, v19, v18
	v_max_f32_e32 v6, v6, v6
	s_waitcnt lgkmcnt(0)
	v_max_f32_e32 v5, v5, v5
	v_med3_f32 v6, v6, s77, v166
	v_med3_f32 v5, v5, s77, v166
	v_cvt_pk_fp8_f32 v20, v6, v5 op_sel:[0,0,1]
	global_store_dword v[2:3], v20, off offset:32
.LBB0_861:
	s_or_b64 exec, exec, s[0:1]
	v_mul_f32_e32 v19, v23, v4
	s_nop 1
	v_mov_b32_dpp v18, v19 quad_perm:[1,0,3,2] row_mask:0xf bank_mask:0xf
	s_nop 1
	v_mov_b32_dpp v6, v19 quad_perm:[2,3,0,1] row_mask:0xf bank_mask:0xf
	s_waitcnt lgkmcnt(0)
	s_nop 1
	v_mov_b32_dpp v5, v18 quad_perm:[2,3,0,1] row_mask:0xf bank_mask:0xf
	s_and_saveexec_b64 s[0:1], vcc
	s_cbranch_execz .LBB0_863
	v_max_f32_e32 v19, v19, v19
	v_max_f32_e32 v18, v18, v18
	v_med3_f32 v19, v19, s77, v166
	v_med3_f32 v18, v18, s77, v166
	v_mov_b32_e32 v20, v149
	v_cvt_pk_fp8_f32 v20, v19, v18
	v_max_f32_e32 v6, v6, v6
	s_waitcnt lgkmcnt(0)
	v_max_f32_e32 v5, v5, v5
	v_med3_f32 v6, v6, s77, v166
	v_med3_f32 v5, v5, s77, v166
	v_cvt_pk_fp8_f32 v20, v6, v5 op_sel:[0,0,1]
	global_store_dword v[2:3], v20, off offset:64
.LBB0_863:
	s_or_b64 exec, exec, s[0:1]
	v_mul_f32_e32 v7, v7, v4
	s_nop 1
	v_mov_b32_dpp v6, v7 quad_perm:[1,0,3,2] row_mask:0xf bank_mask:0xf
	s_waitcnt lgkmcnt(0)
	s_nop 1
	v_mov_b32_dpp v5, v7 quad_perm:[2,3,0,1] row_mask:0xf bank_mask:0xf
	s_nop 1
	v_mov_b32_dpp v4, v6 quad_perm:[2,3,0,1] row_mask:0xf bank_mask:0xf
	s_and_saveexec_b64 s[0:1], vcc
	s_cbranch_execz .LBB0_865
	v_max_f32_e32 v7, v7, v7
	v_max_f32_e32 v6, v6, v6
	v_med3_f32 v7, v7, s77, v166
	v_med3_f32 v6, v6, s77, v166
	v_mov_b32_e32 v18, v149
	v_cvt_pk_fp8_f32 v18, v7, v6
	s_waitcnt lgkmcnt(0)
	v_max_f32_e32 v5, v5, v5
	v_max_f32_e32 v4, v4, v4
	v_med3_f32 v5, v5, s77, v166
	v_med3_f32 v4, v4, s77, v166
	v_cvt_pk_fp8_f32 v18, v5, v4 op_sel:[0,0,1]
	global_store_dword v[2:3], v18, off offset:96
.LBB0_865:
	s_or_b64 exec, exec, s[0:1]
	ds_read_b32 v2, v72 offset:168
	s_waitcnt lgkmcnt(0)
	v_mul_f32_e32 v4, 0x41800000, v2
	v_mul_f32_e32 v18, v56, v4
	s_nop 1
	v_mov_b32_dpp v7, v18 quad_perm:[1,0,3,2] row_mask:0xf bank_mask:0xf
	s_nop 1
	v_mov_b32_dpp v6, v18 quad_perm:[2,3,0,1] row_mask:0xf bank_mask:0xf
	v_lshlrev_b64 v[2:3], 11, v[66:67]
	v_lshl_add_u64 v[2:3], v[68:69], 0, v[2:3]
	v_lshl_add_u64 v[2:3], v[2:3], 0, s[22:23]
	s_waitcnt lgkmcnt(0)
	s_nop 1
	v_mov_b32_dpp v5, v7 quad_perm:[2,3,0,1] row_mask:0xf bank_mask:0xf
	s_and_saveexec_b64 s[0:1], vcc
	s_cbranch_execz .LBB0_867
	v_max_f32_e32 v18, v18, v18
	v_max_f32_e32 v7, v7, v7
	v_med3_f32 v18, v18, s77, v166
	v_med3_f32 v7, v7, s77, v166
	v_mov_b32_e32 v19, v149
	v_cvt_pk_fp8_f32 v19, v18, v7
	v_max_f32_e32 v6, v6, v6
	s_waitcnt lgkmcnt(0)
	v_max_f32_e32 v5, v5, v5
	v_med3_f32 v6, v6, s77, v166
	v_med3_f32 v5, v5, s77, v166
	v_cvt_pk_fp8_f32 v19, v6, v5 op_sel:[0,0,1]
	global_store_dword v[2:3], v19, off
.LBB0_867:
	s_or_b64 exec, exec, s[0:1]
	v_mul_f32_e32 v18, v40, v4
	s_nop 1
	v_mov_b32_dpp v7, v18 quad_perm:[1,0,3,2] row_mask:0xf bank_mask:0xf
	s_nop 1
	v_mov_b32_dpp v6, v18 quad_perm:[2,3,0,1] row_mask:0xf bank_mask:0xf
	s_waitcnt lgkmcnt(0)
	s_nop 1
	v_mov_b32_dpp v5, v7 quad_perm:[2,3,0,1] row_mask:0xf bank_mask:0xf
	s_and_saveexec_b64 s[0:1], vcc
	s_cbranch_execz .LBB0_869
	v_max_f32_e32 v18, v18, v18
	v_max_f32_e32 v7, v7, v7
	v_med3_f32 v18, v18, s77, v166
	v_med3_f32 v7, v7, s77, v166
	v_mov_b32_e32 v19, v149
	v_cvt_pk_fp8_f32 v19, v18, v7
	v_max_f32_e32 v6, v6, v6
	s_waitcnt lgkmcnt(0)
	v_max_f32_e32 v5, v5, v5
	v_med3_f32 v6, v6, s77, v166
	v_med3_f32 v5, v5, s77, v166
	v_cvt_pk_fp8_f32 v19, v6, v5 op_sel:[0,0,1]
	global_store_dword v[2:3], v19, off offset:32
.LBB0_869:
	s_or_b64 exec, exec, s[0:1]
	v_mul_f32_e32 v18, v24, v4
	s_nop 1
	v_mov_b32_dpp v7, v18 quad_perm:[1,0,3,2] row_mask:0xf bank_mask:0xf
	s_nop 1
	v_mov_b32_dpp v6, v18 quad_perm:[2,3,0,1] row_mask:0xf bank_mask:0xf
	s_waitcnt lgkmcnt(0)
	s_nop 1
	v_mov_b32_dpp v5, v7 quad_perm:[2,3,0,1] row_mask:0xf bank_mask:0xf
	s_and_saveexec_b64 s[0:1], vcc
	s_cbranch_execz .LBB0_871
	v_max_f32_e32 v18, v18, v18
	v_max_f32_e32 v7, v7, v7
	v_med3_f32 v18, v18, s77, v166
	v_med3_f32 v7, v7, s77, v166
	v_mov_b32_e32 v19, v149
	v_cvt_pk_fp8_f32 v19, v18, v7
	v_max_f32_e32 v6, v6, v6
	s_waitcnt lgkmcnt(0)
	v_max_f32_e32 v5, v5, v5
	v_med3_f32 v6, v6, s77, v166
	v_med3_f32 v5, v5, s77, v166
	v_cvt_pk_fp8_f32 v19, v6, v5 op_sel:[0,0,1]
	global_store_dword v[2:3], v19, off offset:64
.LBB0_871:
	s_or_b64 exec, exec, s[0:1]
	v_mul_f32_e32 v7, v8, v4
	s_nop 1
	v_mov_b32_dpp v6, v7 quad_perm:[1,0,3,2] row_mask:0xf bank_mask:0xf
	s_waitcnt lgkmcnt(0)
	s_nop 1
	v_mov_b32_dpp v5, v7 quad_perm:[2,3,0,1] row_mask:0xf bank_mask:0xf
	s_nop 1
	v_mov_b32_dpp v4, v6 quad_perm:[2,3,0,1] row_mask:0xf bank_mask:0xf
	s_and_saveexec_b64 s[0:1], vcc
	s_cbranch_execz .LBB0_873
	v_max_f32_e32 v7, v7, v7
	v_max_f32_e32 v6, v6, v6
	v_med3_f32 v7, v7, s77, v166
	v_med3_f32 v6, v6, s77, v166
	v_mov_b32_e32 v8, v149
	v_cvt_pk_fp8_f32 v8, v7, v6
	s_waitcnt lgkmcnt(0)
	v_max_f32_e32 v5, v5, v5
	v_max_f32_e32 v4, v4, v4
	v_med3_f32 v5, v5, s77, v166
	v_med3_f32 v4, v4, s77, v166
	v_cvt_pk_fp8_f32 v8, v5, v4 op_sel:[0,0,1]
	global_store_dword v[2:3], v8, off offset:96
.LBB0_873:
	s_or_b64 exec, exec, s[0:1]
	ds_read_b32 v2, v72 offset:172
	s_waitcnt lgkmcnt(0)
	v_mul_f32_e32 v4, 0x41800000, v2
	v_mul_f32_e32 v8, v57, v4
	s_nop 1
	v_mov_b32_dpp v7, v8 quad_perm:[1,0,3,2] row_mask:0xf bank_mask:0xf
	s_nop 1
	v_mov_b32_dpp v6, v8 quad_perm:[2,3,0,1] row_mask:0xf bank_mask:0xf
	v_lshlrev_b64 v[2:3], 11, v[66:67]
	v_lshl_add_u64 v[2:3], v[68:69], 0, v[2:3]
	v_lshl_add_u64 v[2:3], v[2:3], 0, s[24:25]
	s_waitcnt lgkmcnt(0)
	s_nop 1
	v_mov_b32_dpp v5, v7 quad_perm:[2,3,0,1] row_mask:0xf bank_mask:0xf
	s_and_saveexec_b64 s[0:1], vcc
	s_cbranch_execz .LBB0_875
	v_max_f32_e32 v8, v8, v8
	v_max_f32_e32 v7, v7, v7
	v_med3_f32 v8, v8, s77, v166
	v_med3_f32 v7, v7, s77, v166
	v_mov_b32_e32 v18, v149
	v_cvt_pk_fp8_f32 v18, v8, v7
	v_max_f32_e32 v6, v6, v6
	s_waitcnt lgkmcnt(0)
	v_max_f32_e32 v5, v5, v5
	v_med3_f32 v6, v6, s77, v166
	v_med3_f32 v5, v5, s77, v166
	v_cvt_pk_fp8_f32 v18, v6, v5 op_sel:[0,0,1]
	global_store_dword v[2:3], v18, off
.LBB0_875:
	s_or_b64 exec, exec, s[0:1]
	v_mul_f32_e32 v8, v41, v4
	s_nop 1
	v_mov_b32_dpp v7, v8 quad_perm:[1,0,3,2] row_mask:0xf bank_mask:0xf
	s_nop 1
	v_mov_b32_dpp v6, v8 quad_perm:[2,3,0,1] row_mask:0xf bank_mask:0xf
	s_waitcnt lgkmcnt(0)
	s_nop 1
	v_mov_b32_dpp v5, v7 quad_perm:[2,3,0,1] row_mask:0xf bank_mask:0xf
	s_and_saveexec_b64 s[0:1], vcc
	s_cbranch_execz .LBB0_877
	v_max_f32_e32 v8, v8, v8
	v_max_f32_e32 v7, v7, v7
	v_med3_f32 v8, v8, s77, v166
	v_med3_f32 v7, v7, s77, v166
	v_mov_b32_e32 v18, v149
	v_cvt_pk_fp8_f32 v18, v8, v7
	v_max_f32_e32 v6, v6, v6
	s_waitcnt lgkmcnt(0)
	v_max_f32_e32 v5, v5, v5
	v_med3_f32 v6, v6, s77, v166
	v_med3_f32 v5, v5, s77, v166
	v_cvt_pk_fp8_f32 v18, v6, v5 op_sel:[0,0,1]
	global_store_dword v[2:3], v18, off offset:32
.LBB0_877:
	s_or_b64 exec, exec, s[0:1]
	v_mul_f32_e32 v8, v25, v4
	s_nop 1
	v_mov_b32_dpp v7, v8 quad_perm:[1,0,3,2] row_mask:0xf bank_mask:0xf
	s_nop 1
	v_mov_b32_dpp v6, v8 quad_perm:[2,3,0,1] row_mask:0xf bank_mask:0xf
	s_waitcnt lgkmcnt(0)
	s_nop 1
	v_mov_b32_dpp v5, v7 quad_perm:[2,3,0,1] row_mask:0xf bank_mask:0xf
	s_and_saveexec_b64 s[0:1], vcc
	s_cbranch_execz .LBB0_879
	v_max_f32_e32 v8, v8, v8
	v_max_f32_e32 v7, v7, v7
	v_med3_f32 v8, v8, s77, v166
	v_med3_f32 v7, v7, s77, v166
	v_mov_b32_e32 v18, v149
	v_cvt_pk_fp8_f32 v18, v8, v7
	v_max_f32_e32 v6, v6, v6
	s_waitcnt lgkmcnt(0)
	v_max_f32_e32 v5, v5, v5
	v_med3_f32 v6, v6, s77, v166
	v_med3_f32 v5, v5, s77, v166
	v_cvt_pk_fp8_f32 v18, v6, v5 op_sel:[0,0,1]
	global_store_dword v[2:3], v18, off offset:64
.LBB0_879:
	s_or_b64 exec, exec, s[0:1]
	v_mul_f32_e32 v7, v9, v4
	s_nop 1
	v_mov_b32_dpp v6, v7 quad_perm:[1,0,3,2] row_mask:0xf bank_mask:0xf
	s_waitcnt lgkmcnt(0)
	s_nop 1
	v_mov_b32_dpp v5, v7 quad_perm:[2,3,0,1] row_mask:0xf bank_mask:0xf
	s_nop 1
	v_mov_b32_dpp v4, v6 quad_perm:[2,3,0,1] row_mask:0xf bank_mask:0xf
	s_and_saveexec_b64 s[0:1], vcc
	s_cbranch_execz .LBB0_881
	v_max_f32_e32 v7, v7, v7
	v_max_f32_e32 v6, v6, v6
	v_med3_f32 v7, v7, s77, v166
	v_med3_f32 v6, v6, s77, v166
	v_mov_b32_e32 v8, v149
	v_cvt_pk_fp8_f32 v8, v7, v6
	s_waitcnt lgkmcnt(0)
	v_max_f32_e32 v5, v5, v5
	v_max_f32_e32 v4, v4, v4
	v_med3_f32 v5, v5, s77, v166
	v_med3_f32 v4, v4, s77, v166
	v_cvt_pk_fp8_f32 v8, v5, v4 op_sel:[0,0,1]
	global_store_dword v[2:3], v8, off offset:96
.LBB0_881:
	s_or_b64 exec, exec, s[0:1]
	ds_read_b32 v2, v72 offset:192
	s_waitcnt lgkmcnt(0)
	v_mul_f32_e32 v4, 0x41800000, v2
	v_mul_f32_e32 v8, v58, v4
	s_nop 1
	v_mov_b32_dpp v7, v8 quad_perm:[1,0,3,2] row_mask:0xf bank_mask:0xf
	s_nop 1
	v_mov_b32_dpp v6, v8 quad_perm:[2,3,0,1] row_mask:0xf bank_mask:0xf
	v_lshlrev_b64 v[2:3], 11, v[66:67]
	v_lshl_add_u64 v[2:3], v[68:69], 0, v[2:3]
	v_lshl_add_u64 v[2:3], v[2:3], 0, s[26:27]
	s_waitcnt lgkmcnt(0)
	s_nop 1
	v_mov_b32_dpp v5, v7 quad_perm:[2,3,0,1] row_mask:0xf bank_mask:0xf
	s_and_saveexec_b64 s[0:1], vcc
	s_cbranch_execz .LBB0_883
	v_max_f32_e32 v8, v8, v8
	v_max_f32_e32 v7, v7, v7
	v_med3_f32 v8, v8, s77, v166
	v_med3_f32 v7, v7, s77, v166
	v_mov_b32_e32 v9, v149
	v_cvt_pk_fp8_f32 v9, v8, v7
	v_max_f32_e32 v6, v6, v6
	s_waitcnt lgkmcnt(0)
	v_max_f32_e32 v5, v5, v5
	v_med3_f32 v6, v6, s77, v166
	v_med3_f32 v5, v5, s77, v166
	v_cvt_pk_fp8_f32 v9, v6, v5 op_sel:[0,0,1]
	global_store_dword v[2:3], v9, off
.LBB0_883:
	s_or_b64 exec, exec, s[0:1]
	v_mul_f32_e32 v8, v42, v4
	s_nop 1
	v_mov_b32_dpp v7, v8 quad_perm:[1,0,3,2] row_mask:0xf bank_mask:0xf
	s_nop 1
	v_mov_b32_dpp v6, v8 quad_perm:[2,3,0,1] row_mask:0xf bank_mask:0xf
	s_waitcnt lgkmcnt(0)
	s_nop 1
	v_mov_b32_dpp v5, v7 quad_perm:[2,3,0,1] row_mask:0xf bank_mask:0xf
	s_and_saveexec_b64 s[0:1], vcc
	s_cbranch_execz .LBB0_885
	v_max_f32_e32 v8, v8, v8
	v_max_f32_e32 v7, v7, v7
	v_med3_f32 v8, v8, s77, v166
	v_med3_f32 v7, v7, s77, v166
	v_mov_b32_e32 v9, v149
	v_cvt_pk_fp8_f32 v9, v8, v7
	v_max_f32_e32 v6, v6, v6
	s_waitcnt lgkmcnt(0)
	v_max_f32_e32 v5, v5, v5
	v_med3_f32 v6, v6, s77, v166
	v_med3_f32 v5, v5, s77, v166
	v_cvt_pk_fp8_f32 v9, v6, v5 op_sel:[0,0,1]
	global_store_dword v[2:3], v9, off offset:32
.LBB0_885:
	s_or_b64 exec, exec, s[0:1]
	v_mul_f32_e32 v8, v26, v4
	s_nop 1
	v_mov_b32_dpp v7, v8 quad_perm:[1,0,3,2] row_mask:0xf bank_mask:0xf
	s_nop 1
	v_mov_b32_dpp v6, v8 quad_perm:[2,3,0,1] row_mask:0xf bank_mask:0xf
	s_waitcnt lgkmcnt(0)
	s_nop 1
	v_mov_b32_dpp v5, v7 quad_perm:[2,3,0,1] row_mask:0xf bank_mask:0xf
	s_and_saveexec_b64 s[0:1], vcc
	s_cbranch_execz .LBB0_887
	v_max_f32_e32 v8, v8, v8
	v_max_f32_e32 v7, v7, v7
	v_med3_f32 v8, v8, s77, v166
	v_med3_f32 v7, v7, s77, v166
	v_mov_b32_e32 v9, v149
	v_cvt_pk_fp8_f32 v9, v8, v7
	v_max_f32_e32 v6, v6, v6
	s_waitcnt lgkmcnt(0)
	v_max_f32_e32 v5, v5, v5
	v_med3_f32 v6, v6, s77, v166
	v_med3_f32 v5, v5, s77, v166
	v_cvt_pk_fp8_f32 v9, v6, v5 op_sel:[0,0,1]
	global_store_dword v[2:3], v9, off offset:64
.LBB0_887:
	s_or_b64 exec, exec, s[0:1]
	v_mul_f32_e32 v7, v10, v4
	s_nop 1
	v_mov_b32_dpp v6, v7 quad_perm:[1,0,3,2] row_mask:0xf bank_mask:0xf
	s_waitcnt lgkmcnt(0)
	s_nop 1
	v_mov_b32_dpp v5, v7 quad_perm:[2,3,0,1] row_mask:0xf bank_mask:0xf
	s_nop 1
	v_mov_b32_dpp v4, v6 quad_perm:[2,3,0,1] row_mask:0xf bank_mask:0xf
	s_and_saveexec_b64 s[0:1], vcc
	s_cbranch_execz .LBB0_889
	v_max_f32_e32 v7, v7, v7
	v_max_f32_e32 v6, v6, v6
	v_med3_f32 v7, v7, s77, v166
	v_med3_f32 v6, v6, s77, v166
	v_mov_b32_e32 v8, v149
	v_cvt_pk_fp8_f32 v8, v7, v6
	s_waitcnt lgkmcnt(0)
	v_max_f32_e32 v5, v5, v5
	v_max_f32_e32 v4, v4, v4
	v_med3_f32 v5, v5, s77, v166
	v_med3_f32 v4, v4, s77, v166
	v_cvt_pk_fp8_f32 v8, v5, v4 op_sel:[0,0,1]
	global_store_dword v[2:3], v8, off offset:96
.LBB0_889:
	s_or_b64 exec, exec, s[0:1]
	ds_read_b32 v2, v72 offset:196
	s_waitcnt lgkmcnt(0)
	v_mul_f32_e32 v4, 0x41800000, v2
	v_mul_f32_e32 v8, v59, v4
	s_nop 1
	v_mov_b32_dpp v7, v8 quad_perm:[1,0,3,2] row_mask:0xf bank_mask:0xf
	s_nop 1
	v_mov_b32_dpp v6, v8 quad_perm:[2,3,0,1] row_mask:0xf bank_mask:0xf
	v_lshlrev_b64 v[2:3], 11, v[66:67]
	v_lshl_add_u64 v[2:3], v[68:69], 0, v[2:3]
	v_lshl_add_u64 v[2:3], v[2:3], 0, s[28:29]
	s_waitcnt lgkmcnt(0)
	s_nop 1
	v_mov_b32_dpp v5, v7 quad_perm:[2,3,0,1] row_mask:0xf bank_mask:0xf
	s_and_saveexec_b64 s[0:1], vcc
	s_cbranch_execz .LBB0_891
	v_max_f32_e32 v8, v8, v8
	v_max_f32_e32 v7, v7, v7
	v_med3_f32 v8, v8, s77, v166
	v_med3_f32 v7, v7, s77, v166
	v_mov_b32_e32 v9, v149
	v_cvt_pk_fp8_f32 v9, v8, v7
	v_max_f32_e32 v6, v6, v6
	s_waitcnt lgkmcnt(0)
	v_max_f32_e32 v5, v5, v5
	v_med3_f32 v6, v6, s77, v166
	v_med3_f32 v5, v5, s77, v166
	v_cvt_pk_fp8_f32 v9, v6, v5 op_sel:[0,0,1]
	global_store_dword v[2:3], v9, off
.LBB0_891:
	s_or_b64 exec, exec, s[0:1]
	v_mul_f32_e32 v8, v43, v4
	s_nop 1
	v_mov_b32_dpp v7, v8 quad_perm:[1,0,3,2] row_mask:0xf bank_mask:0xf
	s_nop 1
	v_mov_b32_dpp v6, v8 quad_perm:[2,3,0,1] row_mask:0xf bank_mask:0xf
	s_waitcnt lgkmcnt(0)
	s_nop 1
	v_mov_b32_dpp v5, v7 quad_perm:[2,3,0,1] row_mask:0xf bank_mask:0xf
	s_and_saveexec_b64 s[0:1], vcc
	s_cbranch_execz .LBB0_893
	v_max_f32_e32 v8, v8, v8
	v_max_f32_e32 v7, v7, v7
	v_med3_f32 v8, v8, s77, v166
	v_med3_f32 v7, v7, s77, v166
	v_mov_b32_e32 v9, v149
	v_cvt_pk_fp8_f32 v9, v8, v7
	v_max_f32_e32 v6, v6, v6
	s_waitcnt lgkmcnt(0)
	v_max_f32_e32 v5, v5, v5
	v_med3_f32 v6, v6, s77, v166
	v_med3_f32 v5, v5, s77, v166
	v_cvt_pk_fp8_f32 v9, v6, v5 op_sel:[0,0,1]
	global_store_dword v[2:3], v9, off offset:32
.LBB0_893:
	s_or_b64 exec, exec, s[0:1]
	v_mul_f32_e32 v8, v27, v4
	s_nop 1
	v_mov_b32_dpp v7, v8 quad_perm:[1,0,3,2] row_mask:0xf bank_mask:0xf
	s_nop 1
	v_mov_b32_dpp v6, v8 quad_perm:[2,3,0,1] row_mask:0xf bank_mask:0xf
	s_waitcnt lgkmcnt(0)
	s_nop 1
	v_mov_b32_dpp v5, v7 quad_perm:[2,3,0,1] row_mask:0xf bank_mask:0xf
	s_and_saveexec_b64 s[0:1], vcc
	s_cbranch_execz .LBB0_895
	v_max_f32_e32 v8, v8, v8
	v_max_f32_e32 v7, v7, v7
	v_med3_f32 v8, v8, s77, v166
	v_med3_f32 v7, v7, s77, v166
	v_mov_b32_e32 v9, v149
	v_cvt_pk_fp8_f32 v9, v8, v7
	v_max_f32_e32 v6, v6, v6
	s_waitcnt lgkmcnt(0)
	v_max_f32_e32 v5, v5, v5
	v_med3_f32 v6, v6, s77, v166
	v_med3_f32 v5, v5, s77, v166
	v_cvt_pk_fp8_f32 v9, v6, v5 op_sel:[0,0,1]
	global_store_dword v[2:3], v9, off offset:64
.LBB0_895:
	s_or_b64 exec, exec, s[0:1]
	v_mul_f32_e32 v7, v11, v4
	s_nop 1
	v_mov_b32_dpp v6, v7 quad_perm:[1,0,3,2] row_mask:0xf bank_mask:0xf
	s_waitcnt lgkmcnt(0)
	s_nop 1
	v_mov_b32_dpp v5, v7 quad_perm:[2,3,0,1] row_mask:0xf bank_mask:0xf
	s_nop 1
	v_mov_b32_dpp v4, v6 quad_perm:[2,3,0,1] row_mask:0xf bank_mask:0xf
	s_and_saveexec_b64 s[0:1], vcc
	s_cbranch_execz .LBB0_897
	v_max_f32_e32 v7, v7, v7
	v_max_f32_e32 v6, v6, v6
	v_med3_f32 v7, v7, s77, v166
	v_med3_f32 v6, v6, s77, v166
	v_mov_b32_e32 v8, v149
	v_cvt_pk_fp8_f32 v8, v7, v6
	s_waitcnt lgkmcnt(0)
	v_max_f32_e32 v5, v5, v5
	v_max_f32_e32 v4, v4, v4
	v_med3_f32 v5, v5, s77, v166
	v_med3_f32 v4, v4, s77, v166
	v_cvt_pk_fp8_f32 v8, v5, v4 op_sel:[0,0,1]
	global_store_dword v[2:3], v8, off offset:96
.LBB0_897:
	s_or_b64 exec, exec, s[0:1]
	ds_read_b32 v2, v72 offset:200
	s_waitcnt lgkmcnt(0)
	v_mul_f32_e32 v4, 0x41800000, v2
	v_mul_f32_e32 v8, v60, v4
	s_nop 1
	v_mov_b32_dpp v7, v8 quad_perm:[1,0,3,2] row_mask:0xf bank_mask:0xf
	s_nop 1
	v_mov_b32_dpp v6, v8 quad_perm:[2,3,0,1] row_mask:0xf bank_mask:0xf
	v_lshlrev_b64 v[2:3], 11, v[66:67]
	v_lshl_add_u64 v[2:3], v[68:69], 0, v[2:3]
	v_lshl_add_u64 v[2:3], v[2:3], 0, s[30:31]
	s_waitcnt lgkmcnt(0)
	s_nop 1
	v_mov_b32_dpp v5, v7 quad_perm:[2,3,0,1] row_mask:0xf bank_mask:0xf
	s_and_saveexec_b64 s[0:1], vcc
	s_cbranch_execz .LBB0_899
	v_max_f32_e32 v8, v8, v8
	v_max_f32_e32 v7, v7, v7
	v_med3_f32 v8, v8, s77, v166
	v_med3_f32 v7, v7, s77, v166
	v_mov_b32_e32 v9, v149
	v_cvt_pk_fp8_f32 v9, v8, v7
	v_max_f32_e32 v6, v6, v6
	s_waitcnt lgkmcnt(0)
	v_max_f32_e32 v5, v5, v5
	v_med3_f32 v6, v6, s77, v166
	v_med3_f32 v5, v5, s77, v166
	v_cvt_pk_fp8_f32 v9, v6, v5 op_sel:[0,0,1]
	global_store_dword v[2:3], v9, off
.LBB0_899:
	s_or_b64 exec, exec, s[0:1]
	v_mul_f32_e32 v8, v44, v4
	s_nop 1
	v_mov_b32_dpp v7, v8 quad_perm:[1,0,3,2] row_mask:0xf bank_mask:0xf
	s_nop 1
	v_mov_b32_dpp v6, v8 quad_perm:[2,3,0,1] row_mask:0xf bank_mask:0xf
	s_waitcnt lgkmcnt(0)
	s_nop 1
	v_mov_b32_dpp v5, v7 quad_perm:[2,3,0,1] row_mask:0xf bank_mask:0xf
	s_and_saveexec_b64 s[0:1], vcc
	s_cbranch_execz .LBB0_901
	v_max_f32_e32 v8, v8, v8
	v_max_f32_e32 v7, v7, v7
	v_med3_f32 v8, v8, s77, v166
	v_med3_f32 v7, v7, s77, v166
	v_mov_b32_e32 v9, v149
	v_cvt_pk_fp8_f32 v9, v8, v7
	v_max_f32_e32 v6, v6, v6
	s_waitcnt lgkmcnt(0)
	v_max_f32_e32 v5, v5, v5
	v_med3_f32 v6, v6, s77, v166
	v_med3_f32 v5, v5, s77, v166
	v_cvt_pk_fp8_f32 v9, v6, v5 op_sel:[0,0,1]
	global_store_dword v[2:3], v9, off offset:32
.LBB0_901:
	s_or_b64 exec, exec, s[0:1]
	v_mul_f32_e32 v8, v28, v4
	s_nop 1
	v_mov_b32_dpp v7, v8 quad_perm:[1,0,3,2] row_mask:0xf bank_mask:0xf
	s_nop 1
	v_mov_b32_dpp v6, v8 quad_perm:[2,3,0,1] row_mask:0xf bank_mask:0xf
	s_waitcnt lgkmcnt(0)
	s_nop 1
	v_mov_b32_dpp v5, v7 quad_perm:[2,3,0,1] row_mask:0xf bank_mask:0xf
	s_and_saveexec_b64 s[0:1], vcc
	s_cbranch_execz .LBB0_903
	v_max_f32_e32 v8, v8, v8
	v_max_f32_e32 v7, v7, v7
	v_med3_f32 v8, v8, s77, v166
	v_med3_f32 v7, v7, s77, v166
	v_mov_b32_e32 v9, v149
	v_cvt_pk_fp8_f32 v9, v8, v7
	v_max_f32_e32 v6, v6, v6
	s_waitcnt lgkmcnt(0)
	v_max_f32_e32 v5, v5, v5
	v_med3_f32 v6, v6, s77, v166
	v_med3_f32 v5, v5, s77, v166
	v_cvt_pk_fp8_f32 v9, v6, v5 op_sel:[0,0,1]
	global_store_dword v[2:3], v9, off offset:64
.LBB0_903:
	s_or_b64 exec, exec, s[0:1]
	v_mul_f32_e32 v7, v12, v4
	s_nop 1
	v_mov_b32_dpp v6, v7 quad_perm:[1,0,3,2] row_mask:0xf bank_mask:0xf
	s_waitcnt lgkmcnt(0)
	s_nop 1
	v_mov_b32_dpp v5, v7 quad_perm:[2,3,0,1] row_mask:0xf bank_mask:0xf
	s_nop 1
	v_mov_b32_dpp v4, v6 quad_perm:[2,3,0,1] row_mask:0xf bank_mask:0xf
	s_and_saveexec_b64 s[0:1], vcc
	s_cbranch_execz .LBB0_905
	v_max_f32_e32 v7, v7, v7
	v_max_f32_e32 v6, v6, v6
	v_med3_f32 v7, v7, s77, v166
	v_med3_f32 v6, v6, s77, v166
	v_mov_b32_e32 v8, v149
	v_cvt_pk_fp8_f32 v8, v7, v6
	s_waitcnt lgkmcnt(0)
	v_max_f32_e32 v5, v5, v5
	v_max_f32_e32 v4, v4, v4
	v_med3_f32 v5, v5, s77, v166
	v_med3_f32 v4, v4, s77, v166
	v_cvt_pk_fp8_f32 v8, v5, v4 op_sel:[0,0,1]
	global_store_dword v[2:3], v8, off offset:96
.LBB0_905:
	s_or_b64 exec, exec, s[0:1]
	ds_read_b32 v2, v72 offset:204
	s_waitcnt lgkmcnt(0)
	v_mul_f32_e32 v4, 0x41800000, v2
	v_mul_f32_e32 v8, v61, v4
	s_nop 1
	v_mov_b32_dpp v7, v8 quad_perm:[1,0,3,2] row_mask:0xf bank_mask:0xf
	s_nop 1
	v_mov_b32_dpp v6, v8 quad_perm:[2,3,0,1] row_mask:0xf bank_mask:0xf
	v_lshlrev_b64 v[2:3], 11, v[66:67]
	v_lshl_add_u64 v[2:3], v[68:69], 0, v[2:3]
	v_lshl_add_u64 v[2:3], v[2:3], 0, s[34:35]
	s_waitcnt lgkmcnt(0)
	s_nop 1
	v_mov_b32_dpp v5, v7 quad_perm:[2,3,0,1] row_mask:0xf bank_mask:0xf
	s_and_saveexec_b64 s[0:1], vcc
	s_cbranch_execz .LBB0_907
	v_max_f32_e32 v8, v8, v8
	v_max_f32_e32 v7, v7, v7
	v_med3_f32 v8, v8, s77, v166
	v_med3_f32 v7, v7, s77, v166
	v_mov_b32_e32 v9, v149
	v_cvt_pk_fp8_f32 v9, v8, v7
	v_max_f32_e32 v6, v6, v6
	s_waitcnt lgkmcnt(0)
	v_max_f32_e32 v5, v5, v5
	v_med3_f32 v6, v6, s77, v166
	v_med3_f32 v5, v5, s77, v166
	v_cvt_pk_fp8_f32 v9, v6, v5 op_sel:[0,0,1]
	global_store_dword v[2:3], v9, off
.LBB0_907:
	s_or_b64 exec, exec, s[0:1]
	v_mul_f32_e32 v8, v45, v4
	s_nop 1
	v_mov_b32_dpp v7, v8 quad_perm:[1,0,3,2] row_mask:0xf bank_mask:0xf
	s_nop 1
	v_mov_b32_dpp v6, v8 quad_perm:[2,3,0,1] row_mask:0xf bank_mask:0xf
	s_waitcnt lgkmcnt(0)
	s_nop 1
	v_mov_b32_dpp v5, v7 quad_perm:[2,3,0,1] row_mask:0xf bank_mask:0xf
	s_and_saveexec_b64 s[0:1], vcc
	s_cbranch_execz .LBB0_909
	v_max_f32_e32 v8, v8, v8
	v_max_f32_e32 v7, v7, v7
	v_med3_f32 v8, v8, s77, v166
	v_med3_f32 v7, v7, s77, v166
	v_mov_b32_e32 v9, v149
	v_cvt_pk_fp8_f32 v9, v8, v7
	v_max_f32_e32 v6, v6, v6
	s_waitcnt lgkmcnt(0)
	v_max_f32_e32 v5, v5, v5
	v_med3_f32 v6, v6, s77, v166
	v_med3_f32 v5, v5, s77, v166
	v_cvt_pk_fp8_f32 v9, v6, v5 op_sel:[0,0,1]
	global_store_dword v[2:3], v9, off offset:32
.LBB0_909:
	s_or_b64 exec, exec, s[0:1]
	v_mul_f32_e32 v8, v29, v4
	s_nop 1
	v_mov_b32_dpp v7, v8 quad_perm:[1,0,3,2] row_mask:0xf bank_mask:0xf
	s_nop 1
	v_mov_b32_dpp v6, v8 quad_perm:[2,3,0,1] row_mask:0xf bank_mask:0xf
	s_waitcnt lgkmcnt(0)
	s_nop 1
	v_mov_b32_dpp v5, v7 quad_perm:[2,3,0,1] row_mask:0xf bank_mask:0xf
	s_and_saveexec_b64 s[0:1], vcc
	s_cbranch_execz .LBB0_911
	v_max_f32_e32 v8, v8, v8
	v_max_f32_e32 v7, v7, v7
	v_med3_f32 v8, v8, s77, v166
	v_med3_f32 v7, v7, s77, v166
	v_mov_b32_e32 v9, v149
	v_cvt_pk_fp8_f32 v9, v8, v7
	v_max_f32_e32 v6, v6, v6
	s_waitcnt lgkmcnt(0)
	v_max_f32_e32 v5, v5, v5
	v_med3_f32 v6, v6, s77, v166
	v_med3_f32 v5, v5, s77, v166
	v_cvt_pk_fp8_f32 v9, v6, v5 op_sel:[0,0,1]
	global_store_dword v[2:3], v9, off offset:64
.LBB0_911:
	s_or_b64 exec, exec, s[0:1]
	v_mul_f32_e32 v7, v13, v4
	s_nop 1
	v_mov_b32_dpp v6, v7 quad_perm:[1,0,3,2] row_mask:0xf bank_mask:0xf
	s_waitcnt lgkmcnt(0)
	s_nop 1
	v_mov_b32_dpp v5, v7 quad_perm:[2,3,0,1] row_mask:0xf bank_mask:0xf
	s_nop 1
	v_mov_b32_dpp v4, v6 quad_perm:[2,3,0,1] row_mask:0xf bank_mask:0xf
	s_and_saveexec_b64 s[0:1], vcc
	s_cbranch_execz .LBB0_913
	v_max_f32_e32 v7, v7, v7
	v_max_f32_e32 v6, v6, v6
	v_med3_f32 v7, v7, s77, v166
	v_med3_f32 v6, v6, s77, v166
	v_mov_b32_e32 v8, v149
	v_cvt_pk_fp8_f32 v8, v7, v6
	s_waitcnt lgkmcnt(0)
	v_max_f32_e32 v5, v5, v5
	v_max_f32_e32 v4, v4, v4
	v_med3_f32 v5, v5, s77, v166
	v_med3_f32 v4, v4, s77, v166
	v_cvt_pk_fp8_f32 v8, v5, v4 op_sel:[0,0,1]
	global_store_dword v[2:3], v8, off offset:96
.LBB0_913:
	s_or_b64 exec, exec, s[0:1]
	ds_read_b32 v2, v72 offset:224
	s_waitcnt lgkmcnt(0)
	v_mul_f32_e32 v4, 0x41800000, v2
	v_mul_f32_e32 v8, v62, v4
	s_nop 1
	v_mov_b32_dpp v7, v8 quad_perm:[1,0,3,2] row_mask:0xf bank_mask:0xf
	s_nop 1
	v_mov_b32_dpp v6, v8 quad_perm:[2,3,0,1] row_mask:0xf bank_mask:0xf
	v_lshlrev_b64 v[2:3], 11, v[66:67]
	v_lshl_add_u64 v[2:3], v[68:69], 0, v[2:3]
	v_lshl_add_u64 v[2:3], v[2:3], 0, s[36:37]
	s_waitcnt lgkmcnt(0)
	s_nop 1
	v_mov_b32_dpp v5, v7 quad_perm:[2,3,0,1] row_mask:0xf bank_mask:0xf
	s_and_saveexec_b64 s[0:1], vcc
	s_cbranch_execz .LBB0_915
	v_max_f32_e32 v8, v8, v8
	v_max_f32_e32 v7, v7, v7
	v_med3_f32 v8, v8, s77, v166
	v_med3_f32 v7, v7, s77, v166
	v_mov_b32_e32 v9, v149
	v_cvt_pk_fp8_f32 v9, v8, v7
	v_max_f32_e32 v6, v6, v6
	s_waitcnt lgkmcnt(0)
	v_max_f32_e32 v5, v5, v5
	v_med3_f32 v6, v6, s77, v166
	v_med3_f32 v5, v5, s77, v166
	v_cvt_pk_fp8_f32 v9, v6, v5 op_sel:[0,0,1]
	global_store_dword v[2:3], v9, off
.LBB0_915:
	s_or_b64 exec, exec, s[0:1]
	v_mul_f32_e32 v8, v46, v4
	s_nop 1
	v_mov_b32_dpp v7, v8 quad_perm:[1,0,3,2] row_mask:0xf bank_mask:0xf
	s_nop 1
	v_mov_b32_dpp v6, v8 quad_perm:[2,3,0,1] row_mask:0xf bank_mask:0xf
	s_waitcnt lgkmcnt(0)
	s_nop 1
	v_mov_b32_dpp v5, v7 quad_perm:[2,3,0,1] row_mask:0xf bank_mask:0xf
	s_and_saveexec_b64 s[0:1], vcc
	s_cbranch_execz .LBB0_917
	v_max_f32_e32 v8, v8, v8
	v_max_f32_e32 v7, v7, v7
	v_med3_f32 v8, v8, s77, v166
	v_med3_f32 v7, v7, s77, v166
	v_mov_b32_e32 v9, v149
	v_cvt_pk_fp8_f32 v9, v8, v7
	v_max_f32_e32 v6, v6, v6
	s_waitcnt lgkmcnt(0)
	v_max_f32_e32 v5, v5, v5
	v_med3_f32 v6, v6, s77, v166
	v_med3_f32 v5, v5, s77, v166
	v_cvt_pk_fp8_f32 v9, v6, v5 op_sel:[0,0,1]
	global_store_dword v[2:3], v9, off offset:32
.LBB0_917:
	s_or_b64 exec, exec, s[0:1]
	v_mul_f32_e32 v8, v30, v4
	s_nop 1
	v_mov_b32_dpp v7, v8 quad_perm:[1,0,3,2] row_mask:0xf bank_mask:0xf
	s_nop 1
	v_mov_b32_dpp v6, v8 quad_perm:[2,3,0,1] row_mask:0xf bank_mask:0xf
	s_waitcnt lgkmcnt(0)
	s_nop 1
	v_mov_b32_dpp v5, v7 quad_perm:[2,3,0,1] row_mask:0xf bank_mask:0xf
	s_and_saveexec_b64 s[0:1], vcc
	s_cbranch_execz .LBB0_919
	v_max_f32_e32 v8, v8, v8
	v_max_f32_e32 v7, v7, v7
	v_med3_f32 v8, v8, s77, v166
	v_med3_f32 v7, v7, s77, v166
	v_mov_b32_e32 v9, v149
	v_cvt_pk_fp8_f32 v9, v8, v7
	v_max_f32_e32 v6, v6, v6
	s_waitcnt lgkmcnt(0)
	v_max_f32_e32 v5, v5, v5
	v_med3_f32 v6, v6, s77, v166
	v_med3_f32 v5, v5, s77, v166
	v_cvt_pk_fp8_f32 v9, v6, v5 op_sel:[0,0,1]
	global_store_dword v[2:3], v9, off offset:64
.LBB0_919:
	s_or_b64 exec, exec, s[0:1]
	v_mul_f32_e32 v7, v14, v4
	s_nop 1
	v_mov_b32_dpp v6, v7 quad_perm:[1,0,3,2] row_mask:0xf bank_mask:0xf
	s_waitcnt lgkmcnt(0)
	s_nop 1
	v_mov_b32_dpp v5, v7 quad_perm:[2,3,0,1] row_mask:0xf bank_mask:0xf
	s_nop 1
	v_mov_b32_dpp v4, v6 quad_perm:[2,3,0,1] row_mask:0xf bank_mask:0xf
	s_and_saveexec_b64 s[0:1], vcc
	s_cbranch_execz .LBB0_921
	v_max_f32_e32 v7, v7, v7
	v_max_f32_e32 v6, v6, v6
	v_med3_f32 v7, v7, s77, v166
	v_med3_f32 v6, v6, s77, v166
	v_mov_b32_e32 v8, v149
	v_cvt_pk_fp8_f32 v8, v7, v6
	s_waitcnt lgkmcnt(0)
	v_max_f32_e32 v5, v5, v5
	v_max_f32_e32 v4, v4, v4
	v_med3_f32 v5, v5, s77, v166
	v_med3_f32 v4, v4, s77, v166
	v_cvt_pk_fp8_f32 v8, v5, v4 op_sel:[0,0,1]
	global_store_dword v[2:3], v8, off offset:96
.LBB0_921:
	s_or_b64 exec, exec, s[0:1]
	ds_read_b32 v2, v72 offset:228
	s_waitcnt lgkmcnt(0)
	v_mul_f32_e32 v4, 0x41800000, v2
	v_mul_f32_e32 v8, v63, v4
	s_nop 1
	v_mov_b32_dpp v7, v8 quad_perm:[1,0,3,2] row_mask:0xf bank_mask:0xf
	s_nop 1
	v_mov_b32_dpp v6, v8 quad_perm:[2,3,0,1] row_mask:0xf bank_mask:0xf
	v_lshlrev_b64 v[2:3], 11, v[66:67]
	v_lshl_add_u64 v[2:3], v[68:69], 0, v[2:3]
	v_lshl_add_u64 v[2:3], v[2:3], 0, s[38:39]
	s_waitcnt lgkmcnt(0)
	s_nop 1
	v_mov_b32_dpp v5, v7 quad_perm:[2,3,0,1] row_mask:0xf bank_mask:0xf
	s_and_saveexec_b64 s[0:1], vcc
	s_cbranch_execz .LBB0_923
	v_max_f32_e32 v8, v8, v8
	v_max_f32_e32 v7, v7, v7
	v_med3_f32 v8, v8, s77, v166
	v_med3_f32 v7, v7, s77, v166
	v_mov_b32_e32 v9, v149
	v_cvt_pk_fp8_f32 v9, v8, v7
	v_max_f32_e32 v6, v6, v6
	s_waitcnt lgkmcnt(0)
	v_max_f32_e32 v5, v5, v5
	v_med3_f32 v6, v6, s77, v166
	v_med3_f32 v5, v5, s77, v166
	v_cvt_pk_fp8_f32 v9, v6, v5 op_sel:[0,0,1]
	global_store_dword v[2:3], v9, off
.LBB0_923:
	s_or_b64 exec, exec, s[0:1]
	v_mul_f32_e32 v8, v47, v4
	s_nop 1
	v_mov_b32_dpp v7, v8 quad_perm:[1,0,3,2] row_mask:0xf bank_mask:0xf
	s_nop 1
	v_mov_b32_dpp v6, v8 quad_perm:[2,3,0,1] row_mask:0xf bank_mask:0xf
	s_waitcnt lgkmcnt(0)
	s_nop 1
	v_mov_b32_dpp v5, v7 quad_perm:[2,3,0,1] row_mask:0xf bank_mask:0xf
	s_and_saveexec_b64 s[0:1], vcc
	s_cbranch_execz .LBB0_925
	v_max_f32_e32 v8, v8, v8
	v_max_f32_e32 v7, v7, v7
	v_med3_f32 v8, v8, s77, v166
	v_med3_f32 v7, v7, s77, v166
	v_mov_b32_e32 v9, v149
	v_cvt_pk_fp8_f32 v9, v8, v7
	v_max_f32_e32 v6, v6, v6
	s_waitcnt lgkmcnt(0)
	v_max_f32_e32 v5, v5, v5
	v_med3_f32 v6, v6, s77, v166
	v_med3_f32 v5, v5, s77, v166
	v_cvt_pk_fp8_f32 v9, v6, v5 op_sel:[0,0,1]
	global_store_dword v[2:3], v9, off offset:32
.LBB0_925:
	s_or_b64 exec, exec, s[0:1]
	v_mul_f32_e32 v8, v31, v4
	s_nop 1
	v_mov_b32_dpp v7, v8 quad_perm:[1,0,3,2] row_mask:0xf bank_mask:0xf
	s_nop 1
	v_mov_b32_dpp v6, v8 quad_perm:[2,3,0,1] row_mask:0xf bank_mask:0xf
	s_waitcnt lgkmcnt(0)
	s_nop 1
	v_mov_b32_dpp v5, v7 quad_perm:[2,3,0,1] row_mask:0xf bank_mask:0xf
	s_and_saveexec_b64 s[0:1], vcc
	s_cbranch_execz .LBB0_927
	v_max_f32_e32 v8, v8, v8
	v_max_f32_e32 v7, v7, v7
	v_med3_f32 v8, v8, s77, v166
	v_med3_f32 v7, v7, s77, v166
	v_mov_b32_e32 v9, v149
	v_cvt_pk_fp8_f32 v9, v8, v7
	v_max_f32_e32 v6, v6, v6
	s_waitcnt lgkmcnt(0)
	v_max_f32_e32 v5, v5, v5
	v_med3_f32 v6, v6, s77, v166
	v_med3_f32 v5, v5, s77, v166
	v_cvt_pk_fp8_f32 v9, v6, v5 op_sel:[0,0,1]
	global_store_dword v[2:3], v9, off offset:64
.LBB0_927:
	s_or_b64 exec, exec, s[0:1]
	v_mul_f32_e32 v7, v15, v4
	s_nop 1
	v_mov_b32_dpp v6, v7 quad_perm:[1,0,3,2] row_mask:0xf bank_mask:0xf
	s_waitcnt lgkmcnt(0)
	s_nop 1
	v_mov_b32_dpp v5, v7 quad_perm:[2,3,0,1] row_mask:0xf bank_mask:0xf
	s_nop 1
	v_mov_b32_dpp v4, v6 quad_perm:[2,3,0,1] row_mask:0xf bank_mask:0xf
	s_and_saveexec_b64 s[0:1], vcc
	s_cbranch_execz .LBB0_929
	v_max_f32_e32 v7, v7, v7
	v_max_f32_e32 v6, v6, v6
	v_med3_f32 v7, v7, s77, v166
	v_med3_f32 v6, v6, s77, v166
	v_mov_b32_e32 v8, v149
	v_cvt_pk_fp8_f32 v8, v7, v6
	s_waitcnt lgkmcnt(0)
	v_max_f32_e32 v5, v5, v5
	v_max_f32_e32 v4, v4, v4
	v_med3_f32 v5, v5, s77, v166
	v_med3_f32 v4, v4, s77, v166
	v_cvt_pk_fp8_f32 v8, v5, v4 op_sel:[0,0,1]
	global_store_dword v[2:3], v8, off offset:96
.LBB0_929:
	s_or_b64 exec, exec, s[0:1]
	ds_read_b32 v2, v72 offset:232
	s_waitcnt lgkmcnt(0)
	v_mul_f32_e32 v4, 0x41800000, v2
	v_mul_f32_e32 v8, v64, v4
	s_nop 1
	v_mov_b32_dpp v7, v8 quad_perm:[1,0,3,2] row_mask:0xf bank_mask:0xf
	s_nop 1
	v_mov_b32_dpp v6, v8 quad_perm:[2,3,0,1] row_mask:0xf bank_mask:0xf
	v_lshlrev_b64 v[2:3], 11, v[66:67]
	v_lshl_add_u64 v[2:3], v[68:69], 0, v[2:3]
	v_lshl_add_u64 v[2:3], v[2:3], 0, s[40:41]
	s_waitcnt lgkmcnt(0)
	s_nop 1
	v_mov_b32_dpp v5, v7 quad_perm:[2,3,0,1] row_mask:0xf bank_mask:0xf
	s_and_saveexec_b64 s[0:1], vcc
	s_cbranch_execz .LBB0_931
	v_max_f32_e32 v8, v8, v8
	v_max_f32_e32 v7, v7, v7
	v_med3_f32 v8, v8, s77, v166
	v_med3_f32 v7, v7, s77, v166
	v_mov_b32_e32 v9, v149
	v_cvt_pk_fp8_f32 v9, v8, v7
	v_max_f32_e32 v6, v6, v6
	s_waitcnt lgkmcnt(0)
	v_max_f32_e32 v5, v5, v5
	v_med3_f32 v6, v6, s77, v166
	v_med3_f32 v5, v5, s77, v166
	v_cvt_pk_fp8_f32 v9, v6, v5 op_sel:[0,0,1]
	global_store_dword v[2:3], v9, off
.LBB0_931:
	s_or_b64 exec, exec, s[0:1]
	v_mul_f32_e32 v8, v48, v4
	s_nop 1
	v_mov_b32_dpp v7, v8 quad_perm:[1,0,3,2] row_mask:0xf bank_mask:0xf
	s_nop 1
	v_mov_b32_dpp v6, v8 quad_perm:[2,3,0,1] row_mask:0xf bank_mask:0xf
	s_waitcnt lgkmcnt(0)
	s_nop 1
	v_mov_b32_dpp v5, v7 quad_perm:[2,3,0,1] row_mask:0xf bank_mask:0xf
	s_and_saveexec_b64 s[0:1], vcc
	s_cbranch_execz .LBB0_933
	v_max_f32_e32 v8, v8, v8
	v_max_f32_e32 v7, v7, v7
	v_med3_f32 v8, v8, s77, v166
	v_med3_f32 v7, v7, s77, v166
	v_mov_b32_e32 v9, v149
	v_cvt_pk_fp8_f32 v9, v8, v7
	v_max_f32_e32 v6, v6, v6
	s_waitcnt lgkmcnt(0)
	v_max_f32_e32 v5, v5, v5
	v_med3_f32 v6, v6, s77, v166
	v_med3_f32 v5, v5, s77, v166
	v_cvt_pk_fp8_f32 v9, v6, v5 op_sel:[0,0,1]
	global_store_dword v[2:3], v9, off offset:32
.LBB0_933:
	s_or_b64 exec, exec, s[0:1]
	v_mul_f32_e32 v8, v32, v4
	s_nop 1
	v_mov_b32_dpp v7, v8 quad_perm:[1,0,3,2] row_mask:0xf bank_mask:0xf
	s_nop 1
	v_mov_b32_dpp v6, v8 quad_perm:[2,3,0,1] row_mask:0xf bank_mask:0xf
	s_waitcnt lgkmcnt(0)
	s_nop 1
	v_mov_b32_dpp v5, v7 quad_perm:[2,3,0,1] row_mask:0xf bank_mask:0xf
	s_and_saveexec_b64 s[0:1], vcc
	s_cbranch_execz .LBB0_935
	v_max_f32_e32 v8, v8, v8
	v_max_f32_e32 v7, v7, v7
	v_med3_f32 v8, v8, s77, v166
	v_med3_f32 v7, v7, s77, v166
	v_mov_b32_e32 v9, v149
	v_cvt_pk_fp8_f32 v9, v8, v7
	v_max_f32_e32 v6, v6, v6
	s_waitcnt lgkmcnt(0)
	v_max_f32_e32 v5, v5, v5
	v_med3_f32 v6, v6, s77, v166
	v_med3_f32 v5, v5, s77, v166
	v_cvt_pk_fp8_f32 v9, v6, v5 op_sel:[0,0,1]
	global_store_dword v[2:3], v9, off offset:64
.LBB0_935:
	s_or_b64 exec, exec, s[0:1]
	v_mul_f32_e32 v7, v16, v4
	s_nop 1
	v_mov_b32_dpp v6, v7 quad_perm:[1,0,3,2] row_mask:0xf bank_mask:0xf
	s_waitcnt lgkmcnt(0)
	s_nop 1
	v_mov_b32_dpp v5, v7 quad_perm:[2,3,0,1] row_mask:0xf bank_mask:0xf
	s_nop 1
	v_mov_b32_dpp v4, v6 quad_perm:[2,3,0,1] row_mask:0xf bank_mask:0xf
	s_and_saveexec_b64 s[0:1], vcc
	s_cbranch_execz .LBB0_937
	v_max_f32_e32 v7, v7, v7
	v_max_f32_e32 v6, v6, v6
	v_med3_f32 v7, v7, s77, v166
	v_med3_f32 v6, v6, s77, v166
	v_mov_b32_e32 v8, v149
	v_cvt_pk_fp8_f32 v8, v7, v6
	s_waitcnt lgkmcnt(0)
	v_max_f32_e32 v5, v5, v5
	v_max_f32_e32 v4, v4, v4
	v_med3_f32 v5, v5, s77, v166
	v_med3_f32 v4, v4, s77, v166
	v_cvt_pk_fp8_f32 v8, v5, v4 op_sel:[0,0,1]
	global_store_dword v[2:3], v8, off offset:96
.LBB0_937:
	s_or_b64 exec, exec, s[0:1]
	ds_read_b32 v2, v72 offset:236
	s_waitcnt lgkmcnt(0)
	v_mul_f32_e32 v4, 0x41800000, v2
	v_mul_f32_e32 v8, v65, v4
	s_nop 1
	v_mov_b32_dpp v7, v8 quad_perm:[1,0,3,2] row_mask:0xf bank_mask:0xf
	s_nop 1
	v_mov_b32_dpp v6, v8 quad_perm:[2,3,0,1] row_mask:0xf bank_mask:0xf
	v_lshlrev_b64 v[2:3], 11, v[66:67]
	v_lshl_add_u64 v[2:3], v[68:69], 0, v[2:3]
	v_lshl_add_u64 v[2:3], v[2:3], 0, s[42:43]
	s_waitcnt lgkmcnt(0)
	s_nop 1
	v_mov_b32_dpp v5, v7 quad_perm:[2,3,0,1] row_mask:0xf bank_mask:0xf
	s_and_saveexec_b64 s[0:1], vcc
	s_cbranch_execz .LBB0_939
	v_max_f32_e32 v8, v8, v8
	v_max_f32_e32 v7, v7, v7
	v_med3_f32 v8, v8, s77, v166
	v_med3_f32 v7, v7, s77, v166
	v_mov_b32_e32 v9, v149
	v_cvt_pk_fp8_f32 v9, v8, v7
	v_max_f32_e32 v6, v6, v6
	s_waitcnt lgkmcnt(0)
	v_max_f32_e32 v5, v5, v5
	v_med3_f32 v6, v6, s77, v166
	v_med3_f32 v5, v5, s77, v166
	v_cvt_pk_fp8_f32 v9, v6, v5 op_sel:[0,0,1]
	global_store_dword v[2:3], v9, off
.LBB0_939:
	s_or_b64 exec, exec, s[0:1]
	v_mul_f32_e32 v8, v49, v4
	s_nop 1
	v_mov_b32_dpp v7, v8 quad_perm:[1,0,3,2] row_mask:0xf bank_mask:0xf
	s_nop 1
	v_mov_b32_dpp v6, v8 quad_perm:[2,3,0,1] row_mask:0xf bank_mask:0xf
	s_waitcnt lgkmcnt(0)
	s_nop 1
	v_mov_b32_dpp v5, v7 quad_perm:[2,3,0,1] row_mask:0xf bank_mask:0xf
	s_and_saveexec_b64 s[0:1], vcc
	s_cbranch_execz .LBB0_941
	v_max_f32_e32 v8, v8, v8
	v_max_f32_e32 v7, v7, v7
	v_med3_f32 v8, v8, s77, v166
	v_med3_f32 v7, v7, s77, v166
	v_mov_b32_e32 v9, v149
	v_cvt_pk_fp8_f32 v9, v8, v7
	v_max_f32_e32 v6, v6, v6
	s_waitcnt lgkmcnt(0)
	v_max_f32_e32 v5, v5, v5
	v_med3_f32 v6, v6, s77, v166
	v_med3_f32 v5, v5, s77, v166
	v_cvt_pk_fp8_f32 v9, v6, v5 op_sel:[0,0,1]
	global_store_dword v[2:3], v9, off offset:32
.LBB0_941:
	s_or_b64 exec, exec, s[0:1]
	v_mul_f32_e32 v8, v33, v4
	s_nop 1
	v_mov_b32_dpp v7, v8 quad_perm:[1,0,3,2] row_mask:0xf bank_mask:0xf
	s_nop 1
	v_mov_b32_dpp v6, v8 quad_perm:[2,3,0,1] row_mask:0xf bank_mask:0xf
	s_waitcnt lgkmcnt(0)
	s_nop 1
	v_mov_b32_dpp v5, v7 quad_perm:[2,3,0,1] row_mask:0xf bank_mask:0xf
	s_and_saveexec_b64 s[0:1], vcc
	s_cbranch_execz .LBB0_943
	v_max_f32_e32 v8, v8, v8
	v_max_f32_e32 v7, v7, v7
	v_med3_f32 v8, v8, s77, v166
	v_med3_f32 v7, v7, s77, v166
	v_mov_b32_e32 v9, v149
	v_cvt_pk_fp8_f32 v9, v8, v7
	v_max_f32_e32 v6, v6, v6
	s_waitcnt lgkmcnt(0)
	v_max_f32_e32 v5, v5, v5
	v_med3_f32 v6, v6, s77, v166
	v_med3_f32 v5, v5, s77, v166
	v_cvt_pk_fp8_f32 v9, v6, v5 op_sel:[0,0,1]
	global_store_dword v[2:3], v9, off offset:64
.LBB0_943:
	s_or_b64 exec, exec, s[0:1]
	v_mul_f32_e32 v7, v17, v4
	s_nop 1
	v_mov_b32_dpp v6, v7 quad_perm:[1,0,3,2] row_mask:0xf bank_mask:0xf
	s_waitcnt lgkmcnt(0)
	s_nop 1
	v_mov_b32_dpp v5, v7 quad_perm:[2,3,0,1] row_mask:0xf bank_mask:0xf
	s_nop 1
	v_mov_b32_dpp v4, v6 quad_perm:[2,3,0,1] row_mask:0xf bank_mask:0xf
	s_and_saveexec_b64 s[0:1], vcc
	s_cbranch_execz .LBB0_945
	v_max_f32_e32 v7, v7, v7
	v_max_f32_e32 v6, v6, v6
	v_med3_f32 v7, v7, s77, v166
	v_med3_f32 v6, v6, s77, v166
	v_mov_b32_e32 v8, v149
	v_cvt_pk_fp8_f32 v8, v7, v6
	s_waitcnt lgkmcnt(0)
	v_max_f32_e32 v5, v5, v5
	v_max_f32_e32 v4, v4, v4
	v_med3_f32 v5, v5, s77, v166
	v_med3_f32 v4, v4, s77, v166
	v_cvt_pk_fp8_f32 v8, v5, v4 op_sel:[0,0,1]
	global_store_dword v[2:3], v8, off offset:96

.LBB0_954:
	v_add_f32_e32 v81, v81, v97
	v_fmac_f32_e32 v81, v176, v96
	v_cvt_pk_bf16_f32 v176, v177, v178
	v_cvt_pk_bf16_f32 v177, v83, v84
	v_cvt_pk_bf16_f32 v178, v85, v86
	v_cvt_pk_bf16_f32 v179, v87, v179
	v_cvt_pk_bf16_f32 v84, v88, v89
	v_cvt_pk_bf16_f32 v85, v90, v91
	v_cvt_pk_bf16_f32 v86, v92, v93
	v_cvt_pk_bf16_f32 v87, v94, v95
	v_cvt_pk_bf16_f32 v66, v66, v67
	v_cvt_pk_bf16_f32 v67, v68, v69
	v_cvt_pk_bf16_f32 v68, v70, v71
	v_cvt_pk_bf16_f32 v69, v72, v82
	v_cvt_pk_bf16_f32 v70, v73, v74
	v_cvt_pk_bf16_f32 v71, v75, v76
	v_cvt_pk_bf16_f32 v72, v77, v78
	v_cvt_pk_bf16_f32 v73, v79, v80
	v_lshl_add_u32 v78, s48, 14, v169
	ds_read_b64_tr_b16 v[74:75], v78 offset:0
	ds_read_b64_tr_b16 v[76:77], v78 offset:0x800
	ds_read_b64_tr_b16 v[88:89], v78 offset:0x1000
	ds_read_b64_tr_b16 v[90:91], v78 offset:0x1800
	ds_read_b64_tr_b16 v[92:93], v78 offset:0x2000
	ds_read_b64_tr_b16 v[94:95], v78 offset:0x2800
	ds_read_b64_tr_b16 v[180:181], v78 offset:0x3000
	ds_read_b64_tr_b16 v[182:183], v78 offset:0x3800
	ds_read_b64_tr_b16 v[184:185], v78 offset:0x200
	ds_read_b64_tr_b16 v[186:187], v78 offset:0xa00
	ds_read_b64_tr_b16 v[188:189], v78 offset:0x1200
	ds_read_b64_tr_b16 v[190:191], v78 offset:0x1a00
	ds_read_b64_tr_b16 v[192:193], v78 offset:0x2200
	ds_read_b64_tr_b16 v[194:195], v78 offset:0x2a00
	ds_read_b64_tr_b16 v[196:197], v78 offset:0x3200
	ds_read_b64_tr_b16 v[198:199], v78 offset:0x3a00
	s_waitcnt lgkmcnt(8)
	v_permlane32_swap_b32_e32 v176, v178
	v_permlane32_swap_b32_e32 v177, v179
	v_permlane32_swap_b32_e32 v84, v86
	v_permlane32_swap_b32_e32 v85, v87
	v_permlane32_swap_b32_e32 v66, v68
	v_permlane32_swap_b32_e32 v67, v69
	v_permlane32_swap_b32_e32 v70, v72
	v_permlane32_swap_b32_e32 v71, v73
	v_mfma_f32_32x32x16_bf16 v[50:65], v[176:179], v[74:77], v[50:65]
	ds_read_b64_tr_b16 v[74:75], v78 offset:0x400
	ds_read_b64_tr_b16 v[76:77], v78 offset:0xc00
	v_mfma_f32_32x32x16_bf16 v[50:65], v[84:87], v[88:91], v[50:65]
	ds_read_b64_tr_b16 v[88:89], v78 offset:0x1400
	ds_read_b64_tr_b16 v[90:91], v78 offset:0x1c00
	v_mfma_f32_32x32x16_bf16 v[50:65], v[66:69], v[92:95], v[50:65]
	ds_read_b64_tr_b16 v[92:93], v78 offset:0x2400
	ds_read_b64_tr_b16 v[94:95], v78 offset:0x2c00
	ds_read_b64_tr_b16 v[200:201], v78 offset:0x3400
	ds_read_b64_tr_b16 v[202:203], v78 offset:0x3c00
	s_waitcnt lgkmcnt(8)
	v_mfma_f32_32x32x16_bf16 v[50:65], v[70:73], v[180:183], v[50:65]
	v_mfma_f32_32x32x16_bf16 v[34:49], v[176:179], v[184:187], v[34:49]
	ds_read_b64_tr_b16 v[180:181], v78 offset:0x600
	ds_read_b64_tr_b16 v[182:183], v78 offset:0xe00
	ds_read_b64_tr_b16 v[184:185], v78 offset:0x1600
	ds_read_b64_tr_b16 v[186:187], v78 offset:0x1e00
	v_mfma_f32_32x32x16_bf16 v[34:49], v[84:87], v[188:191], v[34:49]
	ds_read_b64_tr_b16 v[188:189], v78 offset:0x2600
	ds_read_b64_tr_b16 v[190:191], v78 offset:0x2e00
	v_mfma_f32_32x32x16_bf16 v[34:49], v[66:69], v[192:195], v[34:49]
	ds_read_b64_tr_b16 v[192:193], v78 offset:0x3600
	ds_read_b64_tr_b16 v[194:195], v78 offset:0x3e00
	s_waitcnt lgkmcnt(8)
	v_mfma_f32_32x32x16_bf16 v[34:49], v[70:73], v[196:199], v[34:49]
	v_mfma_f32_32x32x16_bf16 v[18:33], v[176:179], v[74:77], v[18:33]
	s_waitcnt lgkmcnt(0)
	v_mfma_f32_32x32x16_bf16 v[18:33], v[84:87], v[88:91], v[18:33]
	v_mfma_f32_32x32x16_bf16 v[18:33], v[66:69], v[92:95], v[18:33]
	v_mfma_f32_32x32x16_bf16 v[18:33], v[70:73], v[200:203], v[18:33]
	v_mfma_f32_32x32x16_bf16 v[2:17], v[176:179], v[180:183], v[2:17]
	s_add_i32 s47, s47, 64
	s_add_i32 s12, s12, 1
	v_lshl_add_u64 v[150:151], v[150:151], 0, s[14:15]
	v_lshl_add_u64 v[152:153], v[152:153], 0, s[14:15]
	v_lshl_add_u64 v[154:155], v[154:155], 0, s[16:17]
	v_lshl_add_u64 v[156:157], v[156:157], 0, s[16:17]
	v_lshl_add_u64 v[158:159], v[158:159], 0, s[16:17]
	v_mfma_f32_32x32x16_bf16 v[2:17], v[84:87], v[184:187], v[2:17]
	v_subrev_u32_e32 v167, 64, v167
	s_cmp_eq_u32 s54, s47
	v_mfma_f32_32x32x16_bf16 v[2:17], v[66:69], v[188:191], v[2:17]
	v_mfma_f32_32x32x16_bf16 v[2:17], v[70:73], v[192:195], v[2:17]
	s_cbranch_scc1 .LBB0_956
	v_mov_b32_e32 v176, v81
	s_add_i32 s44, s47, 0xe0
	s_cmp_ge_i32 s44, s55
	s_cbranch_scc0 .LBB0_946

.Latt2_drain_nodma:
	s_add_i32 s47, s47, 64
	s_add_i32 s12, s12, 1
	v_lshl_add_u64 v[150:151], v[150:151], 0, s[14:15]
	v_lshl_add_u64 v[152:153], v[152:153], 0, s[14:15]
	v_lshl_add_u64 v[154:155], v[154:155], 0, s[16:17]
	v_lshl_add_u64 v[156:157], v[156:157], 0, s[16:17]
	v_lshl_add_u64 v[158:159], v[158:159], 0, s[16:17]
	s_cmp_eq_u32 s54, s47
	s_cbranch_scc0 .Latt2_drain
	s_branch .LBB0_956

.LBB0_958:
	s_or_b64 exec, exec, s[44:45]
	s_waitcnt lgkmcnt(0)
	s_lshl_b64 s[0:1], s[52:53], 11
	v_ashrrev_i32_e32 v73, 3, v170
	v_and_b32_e32 v66, -4, v73
	v_lshl_add_u32 v72, v66, 2, s65
	ds_read_b32 v67, v72 offset:128
	s_add_u32 s0, s61, s0
	s_addc_u32 s1, s62, s1
	s_add_u32 s0, s0, s79
	v_and_b32_e32 v148, 31, v170
	s_waitcnt lgkmcnt(0)
	v_mul_f32_e32 v74, 0x41800000, v67
	v_mul_f32_e32 v76, v50, v74
	s_nop 1
	v_mov_b32_dpp v75, v76 quad_perm:[1,0,3,2] row_mask:0xf bank_mask:0xf
	v_and_b32_e32 v50, 3, v170
	v_cmp_eq_u32_e32 vcc, 0, v50
	s_nop 1
	v_mov_b32_dpp v77, v76 quad_perm:[2,3,0,1] row_mask:0xf bank_mask:0xf
	s_addc_u32 s1, s1, 0
	s_waitcnt lgkmcnt(0)
	s_nop 1
	v_mov_b32_dpp v50, v75 quad_perm:[2,3,0,1] row_mask:0xf bank_mask:0xf
	v_ashrrev_i32_e32 v67, 31, v66
	v_lshl_add_u64 v[68:69], s[0:1], 0, v[148:149]
	v_lshlrev_b64 v[70:71], 11, v[66:67]
	v_lshl_add_u64 v[70:71], v[68:69], 0, v[70:71]
	s_and_saveexec_b64 s[0:1], vcc
	s_cbranch_execz .LBB0_960
	v_max_f32_e32 v76, v76, v76
	v_max_f32_e32 v75, v75, v75
	v_med3_f32 v76, v76, s77, v166
	v_med3_f32 v75, v75, s77, v166
	v_mov_b32_e32 v78, v149
	v_cvt_pk_fp8_f32 v78, v76, v75
	v_max_f32_e32 v77, v77, v77
	s_waitcnt lgkmcnt(0)
	v_max_f32_e32 v50, v50, v50
	v_med3_f32 v75, v77, s77, v166
	v_med3_f32 v50, v50, s77, v166
	v_cvt_pk_fp8_f32 v78, v75, v50 op_sel:[0,0,1]
	global_store_dword v[70:71], v78, off
.LBB0_960:
	s_or_b64 exec, exec, s[0:1]
	v_mul_f32_e32 v76, v34, v74
	s_nop 1
	v_mov_b32_dpp v75, v76 quad_perm:[1,0,3,2] row_mask:0xf bank_mask:0xf
	s_waitcnt lgkmcnt(0)
	s_nop 1
	v_mov_b32_dpp v50, v76 quad_perm:[2,3,0,1] row_mask:0xf bank_mask:0xf
	s_nop 1
	v_mov_b32_dpp v34, v75 quad_perm:[2,3,0,1] row_mask:0xf bank_mask:0xf
	s_and_saveexec_b64 s[0:1], vcc
	s_cbranch_execz .LBB0_962
	v_max_f32_e32 v76, v76, v76
	v_max_f32_e32 v75, v75, v75
	v_med3_f32 v76, v76, s77, v166
	v_med3_f32 v75, v75, s77, v166
	v_mov_b32_e32 v77, v149
	v_cvt_pk_fp8_f32 v77, v76, v75
	s_waitcnt lgkmcnt(0)
	v_max_f32_e32 v50, v50, v50
	v_max_f32_e32 v34, v34, v34
	v_med3_f32 v50, v50, s77, v166
	v_med3_f32 v34, v34, s77, v166
	v_cvt_pk_fp8_f32 v77, v50, v34 op_sel:[0,0,1]
	global_store_dword v[70:71], v77, off offset:32
.LBB0_962:
	s_or_b64 exec, exec, s[0:1]
	v_mul_f32_e32 v75, v18, v74
	s_waitcnt lgkmcnt(0)
	s_nop 1
	v_mov_b32_dpp v50, v75 quad_perm:[1,0,3,2] row_mask:0xf bank_mask:0xf
	s_nop 1
	v_mov_b32_dpp v34, v75 quad_perm:[2,3,0,1] row_mask:0xf bank_mask:0xf
	s_waitcnt lgkmcnt(0)
	s_nop 1
	v_mov_b32_dpp v18, v50 quad_perm:[2,3,0,1] row_mask:0xf bank_mask:0xf
	s_and_saveexec_b64 s[0:1], vcc
	s_cbranch_execz .LBB0_964
	v_max_f32_e32 v75, v75, v75
	v_max_f32_e32 v50, v50, v50
	v_med3_f32 v75, v75, s77, v166
	v_med3_f32 v50, v50, s77, v166
	v_mov_b32_e32 v76, v149
	v_cvt_pk_fp8_f32 v76, v75, v50
	v_max_f32_e32 v34, v34, v34
	s_waitcnt lgkmcnt(0)
	v_max_f32_e32 v18, v18, v18
	v_med3_f32 v34, v34, s77, v166
	v_med3_f32 v18, v18, s77, v166
	v_cvt_pk_fp8_f32 v76, v34, v18 op_sel:[0,0,1]
	global_store_dword v[70:71], v76, off offset:64
.LBB0_964:
	s_or_b64 exec, exec, s[0:1]
	v_mul_f32_e32 v50, v2, v74
	s_nop 1
	v_mov_b32_dpp v34, v50 quad_perm:[1,0,3,2] row_mask:0xf bank_mask:0xf
	s_waitcnt lgkmcnt(0)
	s_nop 1
	v_mov_b32_dpp v18, v50 quad_perm:[2,3,0,1] row_mask:0xf bank_mask:0xf
	s_nop 1
	v_mov_b32_dpp v2, v34 quad_perm:[2,3,0,1] row_mask:0xf bank_mask:0xf
	s_and_saveexec_b64 s[0:1], vcc
	s_cbranch_execz .LBB0_966
	v_max_f32_e32 v50, v50, v50
	v_max_f32_e32 v34, v34, v34
	v_med3_f32 v50, v50, s77, v166
	v_med3_f32 v34, v34, s77, v166
	v_mov_b32_e32 v74, v149
	v_cvt_pk_fp8_f32 v74, v50, v34
	s_waitcnt lgkmcnt(0)
	v_max_f32_e32 v18, v18, v18
	v_max_f32_e32 v2, v2, v2
	v_med3_f32 v18, v18, s77, v166
	v_med3_f32 v2, v2, s77, v166
	v_cvt_pk_fp8_f32 v74, v18, v2 op_sel:[0,0,1]
	global_store_dword v[70:71], v74, off offset:96
.LBB0_966:
	s_or_b64 exec, exec, s[0:1]
	s_waitcnt lgkmcnt(0)
	ds_read_b32 v2, v72 offset:132
	v_or_b32_e32 v50, 1, v66
	s_waitcnt lgkmcnt(0)
	v_mul_f32_e32 v2, 0x41800000, v2
	v_mul_f32_e32 v71, v51, v2
	s_nop 1
	v_mov_b32_dpp v70, v71 quad_perm:[1,0,3,2] row_mask:0xf bank_mask:0xf
	s_nop 1
	v_mov_b32_dpp v34, v71 quad_perm:[2,3,0,1] row_mask:0xf bank_mask:0xf
	v_ashrrev_i32_e32 v51, 31, v50
	v_lshlrev_b64 v[50:51], 11, v[50:51]
	v_lshl_add_u64 v[50:51], v[68:69], 0, v[50:51]
	s_waitcnt lgkmcnt(0)
	s_nop 1
	v_mov_b32_dpp v18, v70 quad_perm:[2,3,0,1] row_mask:0xf bank_mask:0xf
	s_and_saveexec_b64 s[0:1], vcc
	s_cbranch_execz .LBB0_968
	v_max_f32_e32 v71, v71, v71
	v_max_f32_e32 v70, v70, v70
	v_med3_f32 v71, v71, s77, v166
	v_med3_f32 v70, v70, s77, v166
	v_mov_b32_e32 v74, v149
	v_cvt_pk_fp8_f32 v74, v71, v70
	v_max_f32_e32 v34, v34, v34
	s_waitcnt lgkmcnt(0)
	v_max_f32_e32 v18, v18, v18
	v_med3_f32 v34, v34, s77, v166
	v_med3_f32 v18, v18, s77, v166
	v_cvt_pk_fp8_f32 v74, v34, v18 op_sel:[0,0,1]
	global_store_dword v[50:51], v74, off
.LBB0_968:
	s_or_b64 exec, exec, s[0:1]
	v_mul_f32_e32 v70, v35, v2
	s_nop 1
	v_mov_b32_dpp v35, v70 quad_perm:[1,0,3,2] row_mask:0xf bank_mask:0xf
	s_nop 1
	v_mov_b32_dpp v34, v70 quad_perm:[2,3,0,1] row_mask:0xf bank_mask:0xf
	s_waitcnt lgkmcnt(0)
	s_nop 1
	v_mov_b32_dpp v18, v35 quad_perm:[2,3,0,1] row_mask:0xf bank_mask:0xf
	s_and_saveexec_b64 s[0:1], vcc
	s_cbranch_execz .LBB0_970
	v_max_f32_e32 v70, v70, v70
	v_max_f32_e32 v35, v35, v35
	v_med3_f32 v70, v70, s77, v166
	v_med3_f32 v35, v35, s77, v166
	v_mov_b32_e32 v71, v149
	v_cvt_pk_fp8_f32 v71, v70, v35
	v_max_f32_e32 v34, v34, v34
	s_waitcnt lgkmcnt(0)
	v_max_f32_e32 v18, v18, v18
	v_med3_f32 v34, v34, s77, v166
	v_med3_f32 v18, v18, s77, v166
	v_cvt_pk_fp8_f32 v71, v34, v18 op_sel:[0,0,1]
	global_store_dword v[50:51], v71, off offset:32
.LBB0_970:
	s_or_b64 exec, exec, s[0:1]
	v_mul_f32_e32 v35, v19, v2
	s_nop 1
	v_mov_b32_dpp v34, v35 quad_perm:[1,0,3,2] row_mask:0xf bank_mask:0xf
	s_nop 1
	v_mov_b32_dpp v19, v35 quad_perm:[2,3,0,1] row_mask:0xf bank_mask:0xf
	s_waitcnt lgkmcnt(0)
	s_nop 1
	v_mov_b32_dpp v18, v34 quad_perm:[2,3,0,1] row_mask:0xf bank_mask:0xf
	s_and_saveexec_b64 s[0:1], vcc
	s_cbranch_execz .LBB0_972
	v_max_f32_e32 v35, v35, v35
	v_max_f32_e32 v34, v34, v34
	v_med3_f32 v35, v35, s77, v166
	v_med3_f32 v34, v34, s77, v166
	v_mov_b32_e32 v70, v149
	v_cvt_pk_fp8_f32 v70, v35, v34
	v_max_f32_e32 v19, v19, v19
	s_waitcnt lgkmcnt(0)
	v_max_f32_e32 v18, v18, v18
	v_med3_f32 v19, v19, s77, v166
	v_med3_f32 v18, v18, s77, v166
	v_cvt_pk_fp8_f32 v70, v19, v18 op_sel:[0,0,1]
	global_store_dword v[50:51], v70, off offset:64
.LBB0_972:
	s_or_b64 exec, exec, s[0:1]
	v_mul_f32_e32 v19, v3, v2
	s_waitcnt lgkmcnt(0)
	s_nop 1
	v_mov_b32_dpp v18, v19 quad_perm:[1,0,3,2] row_mask:0xf bank_mask:0xf
	s_nop 1
	v_mov_b32_dpp v3, v19 quad_perm:[2,3,0,1] row_mask:0xf bank_mask:0xf
	s_waitcnt lgkmcnt(0)
	s_nop 1
	v_mov_b32_dpp v2, v18 quad_perm:[2,3,0,1] row_mask:0xf bank_mask:0xf
	s_and_saveexec_b64 s[0:1], vcc
	s_cbranch_execz .LBB0_974
	v_max_f32_e32 v19, v19, v19
	v_max_f32_e32 v18, v18, v18
	v_med3_f32 v19, v19, s77, v166
	v_med3_f32 v18, v18, s77, v166
	v_mov_b32_e32 v34, v149
	v_cvt_pk_fp8_f32 v34, v19, v18
	v_max_f32_e32 v3, v3, v3
	s_waitcnt lgkmcnt(0)
	v_max_f32_e32 v2, v2, v2
	v_med3_f32 v3, v3, s77, v166
	v_med3_f32 v2, v2, s77, v166
	v_cvt_pk_fp8_f32 v34, v3, v2 op_sel:[0,0,1]
	global_store_dword v[50:51], v34, off offset:96
.LBB0_974:
	s_or_b64 exec, exec, s[0:1]
	s_waitcnt lgkmcnt(0)
	ds_read_b32 v2, v72 offset:136
	s_waitcnt lgkmcnt(0)
	v_mul_f32_e32 v18, 0x41800000, v2
	v_mul_f32_e32 v50, v52, v18
	s_nop 1
	v_mov_b32_dpp v35, v50 quad_perm:[1,0,3,2] row_mask:0xf bank_mask:0xf
	s_nop 1
	v_mov_b32_dpp v34, v50 quad_perm:[2,3,0,1] row_mask:0xf bank_mask:0xf
	v_or_b32_e32 v2, 2, v66
	v_ashrrev_i32_e32 v3, 31, v2
	v_lshlrev_b64 v[2:3], 11, v[2:3]
	s_waitcnt lgkmcnt(0)
	s_nop 1
	v_mov_b32_dpp v19, v35 quad_perm:[2,3,0,1] row_mask:0xf bank_mask:0xf
	v_lshl_add_u64 v[2:3], v[68:69], 0, v[2:3]
	s_and_saveexec_b64 s[0:1], vcc
	s_cbranch_execz .LBB0_976
	v_max_f32_e32 v50, v50, v50
	v_max_f32_e32 v35, v35, v35
	v_med3_f32 v50, v50, s77, v166
	v_med3_f32 v35, v35, s77, v166
	v_mov_b32_e32 v51, v149
	v_cvt_pk_fp8_f32 v51, v50, v35
	v_max_f32_e32 v34, v34, v34
	s_waitcnt lgkmcnt(0)
	v_max_f32_e32 v19, v19, v19
	v_med3_f32 v34, v34, s77, v166
	v_med3_f32 v19, v19, s77, v166
	v_cvt_pk_fp8_f32 v51, v34, v19 op_sel:[0,0,1]
	global_store_dword v[2:3], v51, off

.LBB0_1084:
	s_or_b64 exec, exec, s[0:1]
	v_mul_f32_e32 v7, v17, v4
	s_nop 1
	v_mov_b32_dpp v6, v7 quad_perm:[1,0,3,2] row_mask:0xf bank_mask:0xf
	s_waitcnt lgkmcnt(0)
	s_nop 1
	v_mov_b32_dpp v5, v7 quad_perm:[2,3,0,1] row_mask:0xf bank_mask:0xf
	s_nop 1
	v_mov_b32_dpp v4, v6 quad_perm:[2,3,0,1] row_mask:0xf bank_mask:0xf
	s_and_saveexec_b64 s[0:1], vcc
	s_cbranch_execz .LBB0_803
	v_max_f32_e32 v7, v7, v7
	v_max_f32_e32 v6, v6, v6
	v_med3_f32 v7, v7, s77, v166
	v_med3_f32 v6, v6, s77, v166
	v_mov_b32_e32 v8, v149
	v_cvt_pk_fp8_f32 v8, v7, v6
	s_waitcnt lgkmcnt(0)
	v_max_f32_e32 v5, v5, v5
	v_max_f32_e32 v4, v4, v4
	v_med3_f32 v5, v5, s77, v166
	v_med3_f32 v4, v4, s77, v166
	v_cvt_pk_fp8_f32 v8, v5, v4 op_sel:[0,0,1]
	global_store_dword v[2:3], v8, off offset:96
	s_branch .LBB0_803
